# all six GEMM K-loops: tile prefetch (global_load_lds + address arithmetic) issued at the start of each load segment, ahead of the LDS fragment reads; LDS address temporaries renamed onto their last re
# speedup vs baseline: 1.0107x; 1.0069x over previous
.LBB0_194:
	s_add_u32 s34, s92, 0xfffa0080
	s_addc_u32 s35, s93, -1
	s_add_i32 s2, 0, 0x10000
	s_cmp_eq_u32 s1, 12
	s_cselect_b32 s95, s57, s35
	s_cselect_b32 s94, vcc_lo, s34
	s_cselect_b32 s97, s55, s11
	s_cselect_b32 s96, vcc_hi, s10
	s_add_i32 s82, 0, 0x14000
	s_mov_b32 s34, 0xfffe0000
	s_mov_b32 s35, -1
	v_lshl_add_u64 v[168:169], s[92:93], 0, v[154:155]
	v_lshl_add_u64 v[168:169], v[168:169], 0, s[34:35]
	s_add_i32 m0, s89, 0xc000
	s_nop 0
	global_load_lds_dwordx4 v[168:169], off
	s_add_i32 m0, s89, 0xe000
	s_nop 0
	global_load_lds_dwordx4 v154, s[92:93]
	v_add_u32_e32 v146, s68, v174
	v_add_u32_e32 v142, s2, v146
	v_add_u32_e32 v164, s82, v146
	ds_read_b128 v[130:133], v142
	ds_read_b128 v[134:137], v142 offset:1024
	ds_read_b128 v[138:141], v142 offset:2048
	ds_read_b128 v[142:145], v142 offset:3072
	ds_read_b128 v[146:149], v164
	ds_read_b128 v[150:153], v164 offset:1024
	ds_read_b128 v[160:163], v164 offset:2048
	ds_read_b128 v[164:167], v164 offset:3072
	v_add_u32_e32 v159, s69, v174
	ds_read_b128 v[176:179], v159
	ds_read_b128 v[180:183], v159 offset:1024
	ds_read_b128 v[184:187], v159 offset:2048
	ds_read_b128 v[188:191], v159 offset:3072
	ds_read_b128 v[196:199], v159 offset:4096
	ds_read_b128 v[200:203], v159 offset:5120
	ds_read_b128 v[204:207], v159 offset:6144
	ds_read_b128 v[208:211], v159 offset:7168
	s_waitcnt vmcnt(8)
	s_waitcnt lgkmcnt(0)
	s_barrier
	s_setprio 1
	s_waitcnt lgkmcnt(0)
	v_mfma_scale_f32_16x16x128_f8f6f4 v[126:129], v[130:137], v[176:183], v[126:129], v1, v1 op_sel_hi:[0,0,0]
	v_mfma_scale_f32_16x16x128_f8f6f4 v[122:125], v[138:145], v[176:183], v[122:125], v1, v1 op_sel_hi:[0,0,0]
	v_mfma_scale_f32_16x16x128_f8f6f4 v[114:117], v[130:137], v[184:191], v[114:117], v1, v1 op_sel_hi:[0,0,0]
	v_mfma_scale_f32_16x16x128_f8f6f4 v[106:109], v[138:145], v[184:191], v[106:109], v1, v1 op_sel_hi:[0,0,0]
	v_mfma_scale_f32_16x16x128_f8f6f4 v[98:101], v[130:137], v[196:203], v[98:101], v1, v1 op_sel_hi:[0,0,0]
	v_mfma_scale_f32_16x16x128_f8f6f4 v[212:215], v[138:145], v[196:203], v[90:93], v1, v1 op_sel_hi:[0,0,0]
	v_mfma_scale_f32_16x16x128_f8f6f4 v[216:219], v[130:137], v[204:211], v[82:85], v1, v1 op_sel_hi:[0,0,0]
	v_mfma_scale_f32_16x16x128_f8f6f4 v[220:223], v[138:145], v[204:211], v[74:77], v1, v1 op_sel_hi:[0,0,0]
	s_setprio 0
	s_setprio 1
	v_mfma_scale_f32_16x16x128_f8f6f4 v[118:121], v[146:153], v[176:183], v[118:121], v1, v1 op_sel_hi:[0,0,0]
	v_mfma_scale_f32_16x16x128_f8f6f4 v[110:113], v[160:167], v[176:183], v[110:113], v1, v1 op_sel_hi:[0,0,0]
	v_mfma_scale_f32_16x16x128_f8f6f4 v[102:105], v[146:153], v[184:191], v[102:105], v1, v1 op_sel_hi:[0,0,0]
	v_mfma_scale_f32_16x16x128_f8f6f4 v[176:179], v[160:167], v[184:191], v[94:97], v1, v1 op_sel_hi:[0,0,0]
	v_mfma_scale_f32_16x16x128_f8f6f4 v[180:183], v[146:153], v[196:203], v[86:89], v1, v1 op_sel_hi:[0,0,0]
	v_mfma_scale_f32_16x16x128_f8f6f4 v[184:187], v[160:167], v[196:203], v[78:81], v1, v1 op_sel_hi:[0,0,0]
	v_mfma_scale_f32_16x16x128_f8f6f4 v[188:191], v[146:153], v[204:211], v[62:65], v1, v1 op_sel_hi:[0,0,0]
	v_mfma_scale_f32_16x16x128_f8f6f4 v[196:199], v[160:167], v[204:211], v[58:61], v1, v1 op_sel_hi:[0,0,0]
	s_setprio 0
	s_barrier
	v_mov_b32_e32 v159, v155
	v_add_u32_e32 v94, s69, v174
	s_add_i32 s2, s2, s6
	s_nop 1
	s_mov_b32 m0, s2
	v_lshl_add_u64 v[168:169], s[96:97], 0, v[158:159]
	global_load_lds_dwordx4 v158, s[96:97]
	v_lshl_add_u64 v[168:169], v[168:169], 0, s[14:15]
	s_add_i32 m0, s2, 0x2000
	s_add_i32 s2, s82, s6
	global_load_lds_dwordx4 v[168:169], off
	s_mov_b32 m0, s2
	v_lshl_add_u64 v[168:169], s[96:97], 0, v[158:159]
	v_lshl_add_u64 v[170:171], v[168:169], 0, s[16:17]
	global_load_lds_dwordx4 v[170:171], off
	v_lshl_add_u64 v[168:169], v[168:169], 0, s[18:19]
	s_add_i32 m0, s2, 0x2000
	s_nop 0
	global_load_lds_dwordx4 v[168:169], off
	s_mov_b32 m0, s89
	v_lshl_add_u64 v[168:169], s[94:95], 0, v[154:155]
	global_load_lds_dwordx4 v154, s[94:95]
	v_lshl_add_u64 v[168:169], v[168:169], 0, s[14:15]
	s_mov_b32 m0, s91
	s_nop 0
	global_load_lds_dwordx4 v[168:169], off
	ds_read_b128 v[58:61], v94 offset:16384
	ds_read_b128 v[62:65], v94 offset:17408
	ds_read_b128 v[74:77], v94 offset:18432
	ds_read_b128 v[78:81], v94 offset:19456
	ds_read_b128 v[82:85], v94 offset:20480
	ds_read_b128 v[86:89], v94 offset:21504
	ds_read_b128 v[90:93], v94 offset:22528
	ds_read_b128 v[94:97], v94 offset:23552
	s_waitcnt vmcnt(8)
	s_waitcnt lgkmcnt(0)
	s_barrier
	s_setprio 1
	s_waitcnt lgkmcnt(0)
	v_mfma_scale_f32_16x16x128_f8f6f4 v[54:57], v[130:137], v[58:65], v[54:57], v1, v1 op_sel_hi:[0,0,0]
	v_mfma_scale_f32_16x16x128_f8f6f4 v[200:203], v[138:145], v[58:65], v[42:45], v1, v1 op_sel_hi:[0,0,0]
	v_mfma_scale_f32_16x16x128_f8f6f4 v[204:207], v[130:137], v[74:81], v[30:33], v1, v1 op_sel_hi:[0,0,0]
	v_mfma_scale_f32_16x16x128_f8f6f4 v[208:211], v[138:145], v[74:81], v[26:29], v1, v1 op_sel_hi:[0,0,0]
	v_mfma_scale_f32_16x16x128_f8f6f4 v[224:227], v[130:137], v[82:89], v[14:17], v1, v1 op_sel_hi:[0,0,0]
	v_mfma_scale_f32_16x16x128_f8f6f4 v[228:231], v[138:145], v[82:89], v[10:13], v1, v1 op_sel_hi:[0,0,0]
	v_mfma_scale_f32_16x16x128_f8f6f4 v[232:235], v[130:137], v[90:97], v[6:9], v1, v1 op_sel_hi:[0,0,0]
	v_mfma_scale_f32_16x16x128_f8f6f4 v[236:239], v[138:145], v[90:97], v[2:5], v1, v1 op_sel_hi:[0,0,0]
	s_setprio 0
	s_setprio 1
	v_mfma_scale_f32_16x16x128_f8f6f4 v[66:69], v[146:153], v[58:65], v[66:69], v1, v1 op_sel_hi:[0,0,0]
	v_mfma_scale_f32_16x16x128_f8f6f4 v[70:73], v[160:167], v[58:65], v[70:73], v1, v1 op_sel_hi:[0,0,0]
	v_mfma_scale_f32_16x16x128_f8f6f4 v[50:53], v[160:167], v[74:81], v[50:53], v1, v1 op_sel_hi:[0,0,0]
	v_mfma_scale_f32_16x16x128_f8f6f4 v[240:243], v[146:153], v[74:81], v[46:49], v1, v1 op_sel_hi:[0,0,0]
	v_mfma_scale_f32_16x16x128_f8f6f4 v[244:247], v[146:153], v[82:89], v[34:37], v1, v1 op_sel_hi:[0,0,0]
	v_mfma_scale_f32_16x16x128_f8f6f4 v[248:251], v[160:167], v[82:89], v[38:41], v1, v1 op_sel_hi:[0,0,0]
	v_mfma_scale_f32_16x16x128_f8f6f4 v[192:195], v[146:153], v[90:97], v[18:21], v1, v1 op_sel_hi:[0,0,0]
	v_mfma_scale_f32_16x16x128_f8f6f4 v[168:171], v[160:167], v[90:97], v[22:25], v1, v1 op_sel_hi:[0,0,0]
	s_setprio 0
	s_barrier
	s_mov_b32 m0, s7
	v_lshl_add_u64 v[58:59], s[94:95], 0, v[154:155]
	v_lshl_add_u64 v[60:61], v[58:59], 0, s[16:17]
	global_load_lds_dwordx4 v[60:61], off
	v_lshl_add_u64 v[58:59], v[58:59], 0, s[18:19]
	s_mov_b32 m0, s0
	s_nop 0
	global_load_lds_dwordx4 v[58:59], off
	s_add_i32 s2, 0, 0x18000
	v_add_u32_e32 v10, s68, v174
	s_add_i32 s34, 0, 0x1c000
	v_add_u32_e32 v22, s2, v10
	v_add_u32_e32 v10, s34, v10
	ds_read_b128 v[2:5], v22
	ds_read_b128 v[6:9], v22 offset:1024
	ds_read_b128 v[18:21], v22 offset:2048
	ds_read_b128 v[22:25], v22 offset:3072
	ds_read_b128 v[130:133], v10
	ds_read_b128 v[134:137], v10 offset:1024
	ds_read_b128 v[138:141], v10 offset:2048
	ds_read_b128 v[142:145], v10 offset:3072
	v_add_u32_e32 v46, s69, v174
	ds_read_b128 v[10:13], v46 offset:32768
	ds_read_b128 v[14:17], v46 offset:33792
	ds_read_b128 v[26:29], v46 offset:34816
	ds_read_b128 v[30:33], v46 offset:35840
	ds_read_b128 v[34:37], v46 offset:36864
	ds_read_b128 v[38:41], v46 offset:37888
	ds_read_b128 v[42:45], v46 offset:38912
	ds_read_b128 v[46:49], v46 offset:39936
	s_waitcnt vmcnt(8)
	s_waitcnt lgkmcnt(0)
	s_barrier
	s_setprio 1
	s_waitcnt lgkmcnt(0)
	v_mfma_scale_f32_16x16x128_f8f6f4 v[126:129], v[2:9], v[10:17], v[126:129], v1, v1 op_sel_hi:[0,0,0]
	v_mfma_scale_f32_16x16x128_f8f6f4 v[122:125], v[18:25], v[10:17], v[122:125], v1, v1 op_sel_hi:[0,0,0]
	v_mfma_scale_f32_16x16x128_f8f6f4 v[114:117], v[2:9], v[26:33], v[114:117], v1, v1 op_sel_hi:[0,0,0]
	v_mfma_scale_f32_16x16x128_f8f6f4 v[106:109], v[18:25], v[26:33], v[106:109], v1, v1 op_sel_hi:[0,0,0]
	v_mfma_scale_f32_16x16x128_f8f6f4 v[98:101], v[2:9], v[34:41], v[98:101], v1, v1 op_sel_hi:[0,0,0]
	v_mfma_scale_f32_16x16x128_f8f6f4 v[90:93], v[18:25], v[34:41], v[212:215], v1, v1 op_sel_hi:[0,0,0]
	v_mfma_scale_f32_16x16x128_f8f6f4 v[82:85], v[2:9], v[42:49], v[216:219], v1, v1 op_sel_hi:[0,0,0]
	v_mfma_scale_f32_16x16x128_f8f6f4 v[74:77], v[18:25], v[42:49], v[220:223], v1, v1 op_sel_hi:[0,0,0]
	s_setprio 0
	s_setprio 1
	v_mfma_scale_f32_16x16x128_f8f6f4 v[118:121], v[130:137], v[10:17], v[118:121], v1, v1 op_sel_hi:[0,0,0]
	v_mfma_scale_f32_16x16x128_f8f6f4 v[110:113], v[138:145], v[10:17], v[110:113], v1, v1 op_sel_hi:[0,0,0]
	v_mfma_scale_f32_16x16x128_f8f6f4 v[102:105], v[130:137], v[26:33], v[102:105], v1, v1 op_sel_hi:[0,0,0]
	v_mfma_scale_f32_16x16x128_f8f6f4 v[94:97], v[138:145], v[26:33], v[176:179], v1, v1 op_sel_hi:[0,0,0]
	v_mfma_scale_f32_16x16x128_f8f6f4 v[86:89], v[130:137], v[34:41], v[180:183], v1, v1 op_sel_hi:[0,0,0]
	v_mfma_scale_f32_16x16x128_f8f6f4 v[78:81], v[138:145], v[34:41], v[184:187], v1, v1 op_sel_hi:[0,0,0]
	v_mfma_scale_f32_16x16x128_f8f6f4 v[62:65], v[130:137], v[42:49], v[188:191], v1, v1 op_sel_hi:[0,0,0]
	v_mfma_scale_f32_16x16x128_f8f6f4 v[58:61], v[138:145], v[42:49], v[196:199], v1, v1 op_sel_hi:[0,0,0]
	s_setprio 0
	s_barrier
	s_add_i32 s2, s2, s6
	s_mov_b32 m0, s2
	v_lshl_add_u64 v[10:11], s[96:97], 0, v[158:159]
	v_lshl_add_u64 v[12:13], v[10:11], 0, s[20:21]
	global_load_lds_dwordx4 v[12:13], off
	v_lshl_add_u64 v[10:11], v[10:11], 0, s[22:23]
	s_add_i32 m0, s2, 0x2000
	s_add_i32 s2, s34, s6
	global_load_lds_dwordx4 v[10:11], off
	s_mov_b32 m0, s2
	v_lshl_add_u64 v[10:11], s[96:97], 0, v[158:159]
	v_lshl_add_u64 v[12:13], v[10:11], 0, s[24:25]
	global_load_lds_dwordx4 v[12:13], off
	v_lshl_add_u64 v[10:11], v[10:11], 0, s[26:27]
	s_add_i32 m0, s2, 0x2000
	s_nop 0
	global_load_lds_dwordx4 v[10:11], off
	s_mov_b32 m0, s33
	v_lshl_add_u64 v[10:11], s[94:95], 0, v[154:155]
	v_lshl_add_u64 v[12:13], v[10:11], 0, s[20:21]
	global_load_lds_dwordx4 v[12:13], off
	v_lshl_add_u64 v[10:11], v[10:11], 0, s[22:23]
	s_mov_b32 m0, s76
	s_nop 0
	global_load_lds_dwordx4 v[10:11], off
	v_add_u32_e32 v180, s69, v174
	ds_read_b128 v[34:37], v180 offset:49152
	ds_read_b128 v[38:41], v180 offset:50176
	ds_read_b128 v[146:149], v180 offset:51200
	ds_read_b128 v[150:153], v180 offset:52224
	ds_read_b128 v[160:163], v180 offset:53248
	ds_read_b128 v[164:167], v180 offset:54272
	ds_read_b128 v[176:179], v180 offset:55296
	ds_read_b128 v[180:183], v180 offset:56320
	s_waitcnt vmcnt(8)
	s_waitcnt lgkmcnt(0)
	s_barrier
	s_setprio 1
	s_waitcnt lgkmcnt(0)
	v_mfma_scale_f32_16x16x128_f8f6f4 v[54:57], v[2:9], v[34:41], v[54:57], v1, v1 op_sel_hi:[0,0,0]
	v_mfma_scale_f32_16x16x128_f8f6f4 v[42:45], v[18:25], v[34:41], v[200:203], v1, v1 op_sel_hi:[0,0,0]
	v_mfma_scale_f32_16x16x128_f8f6f4 v[30:33], v[2:9], v[146:153], v[204:207], v1, v1 op_sel_hi:[0,0,0]
	v_mfma_scale_f32_16x16x128_f8f6f4 v[26:29], v[18:25], v[146:153], v[208:211], v1, v1 op_sel_hi:[0,0,0]
	v_mfma_scale_f32_16x16x128_f8f6f4 v[14:17], v[2:9], v[160:167], v[224:227], v1, v1 op_sel_hi:[0,0,0]
	v_mfma_scale_f32_16x16x128_f8f6f4 v[10:13], v[18:25], v[160:167], v[228:231], v1, v1 op_sel_hi:[0,0,0]
	v_mfma_scale_f32_16x16x128_f8f6f4 v[6:9], v[2:9], v[176:183], v[232:235], v1, v1 op_sel_hi:[0,0,0]
	v_mfma_scale_f32_16x16x128_f8f6f4 v[2:5], v[18:25], v[176:183], v[236:239], v1, v1 op_sel_hi:[0,0,0]
	s_setprio 0
	s_setprio 1
	v_mfma_scale_f32_16x16x128_f8f6f4 v[66:69], v[130:137], v[34:41], v[66:69], v1, v1 op_sel_hi:[0,0,0]
	v_mfma_scale_f32_16x16x128_f8f6f4 v[70:73], v[138:145], v[34:41], v[70:73], v1, v1 op_sel_hi:[0,0,0]
	v_mfma_scale_f32_16x16x128_f8f6f4 v[46:49], v[130:137], v[146:153], v[240:243], v1, v1 op_sel_hi:[0,0,0]
	v_mfma_scale_f32_16x16x128_f8f6f4 v[50:53], v[138:145], v[146:153], v[50:53], v1, v1 op_sel_hi:[0,0,0]
	v_mfma_scale_f32_16x16x128_f8f6f4 v[34:37], v[130:137], v[160:167], v[244:247], v1, v1 op_sel_hi:[0,0,0]
	v_mfma_scale_f32_16x16x128_f8f6f4 v[38:41], v[138:145], v[160:167], v[248:251], v1, v1 op_sel_hi:[0,0,0]
	v_mfma_scale_f32_16x16x128_f8f6f4 v[18:21], v[130:137], v[176:183], v[192:195], v1, v1 op_sel_hi:[0,0,0]
	v_mfma_scale_f32_16x16x128_f8f6f4 v[22:25], v[138:145], v[176:183], v[168:171], v1, v1 op_sel_hi:[0,0,0]
	s_setprio 0
	s_barrier
	s_add_i32 s1, s1, 2
	s_add_u32 s92, s92, 0x100
	s_addc_u32 s93, s93, 0
	s_add_u32 s10, s10, 0x100
	s_addc_u32 s11, s11, 0
	s_cmp_gt_u32 s1, 13
	s_cbranch_scc0 .LBB0_194
	s_and_b64 vcc, exec, s[64:65]
	s_cbranch_vccz .LBB0_197
	s_barrier

.LBB0_977:
	s_add_u32 s34, s58, 0xfffd0080
	v_add_u32_e32 v46, s84, v1
	v_add_u32_e32 v142, s88, v46
	v_add_u32_e32 v46, s89, v46
	ds_read_b128 v[130:133], v142
	ds_read_b128 v[134:137], v142 offset:1024
	ds_read_b128 v[138:141], v142 offset:2048
	ds_read_b128 v[142:145], v142 offset:3072
	ds_read_b128 v[146:149], v46
	ds_read_b128 v[150:153], v46 offset:1024
	ds_read_b128 v[154:157], v46 offset:2048
	ds_read_b128 v[158:161], v46 offset:3072
	s_addc_u32 s35, s59, -1
	s_cmp_eq_u32 s70, 4
	s_cselect_b32 s61, s38, s35
	s_cselect_b32 s60, s39, s34
	s_cselect_b32 s63, s45, s69
	s_cselect_b32 s62, s47, s68
	s_mov_b32 s34, 0xffff0000
	s_mov_b32 s35, -1
	v_lshl_add_u64 v[46:47], s[58:59], 0, v[196:197]
	v_lshl_add_u64 v[46:47], v[46:47], 0, s[34:35]
	s_add_i32 m0, s64, 0xc000
	s_nop 0
	global_load_lds_dwordx4 v[46:47], off
	s_add_i32 m0, s64, 0xe000
	s_nop 0
	global_load_lds_dwordx4 v196, s[58:59]
	v_add_u32_e32 v190, s85, v1
	ds_read_b128 v[162:165], v190
	ds_read_b128 v[166:169], v190 offset:1024
	ds_read_b128 v[170:173], v190 offset:2048
	ds_read_b128 v[174:177], v190 offset:3072
	ds_read_b128 v[178:181], v190 offset:4096
	ds_read_b128 v[182:185], v190 offset:5120
	ds_read_b128 v[186:189], v190 offset:6144
	ds_read_b128 v[190:193], v190 offset:7168
	s_waitcnt vmcnt(8)
	s_waitcnt lgkmcnt(0)
	s_barrier
	s_setprio 1
	s_waitcnt lgkmcnt(0)
	v_mfma_scale_f32_16x16x128_f8f6f4 v[94:97], v[130:137], v[162:169], v[94:97], v195, v195 op_sel_hi:[0,0,0]
	v_mfma_scale_f32_16x16x128_f8f6f4 v[90:93], v[138:145], v[162:169], v[90:93], v195, v195 op_sel_hi:[0,0,0]
	v_mfma_scale_f32_16x16x128_f8f6f4 v[86:89], v[130:137], v[170:177], v[86:89], v195, v195 op_sel_hi:[0,0,0]
	v_mfma_scale_f32_16x16x128_f8f6f4 v[82:85], v[138:145], v[170:177], v[82:85], v195, v195 op_sel_hi:[0,0,0]
	v_mfma_scale_f32_16x16x128_f8f6f4 v[78:81], v[130:137], v[178:185], v[78:81], v195, v195 op_sel_hi:[0,0,0]
	v_mfma_scale_f32_16x16x128_f8f6f4 v[204:207], v[138:145], v[178:185], v[74:77], v195, v195 op_sel_hi:[0,0,0]
	v_mfma_scale_f32_16x16x128_f8f6f4 v[208:211], v[130:137], v[186:193], v[70:73], v195, v195 op_sel_hi:[0,0,0]
	v_mfma_scale_f32_16x16x128_f8f6f4 v[212:215], v[138:145], v[186:193], v[66:69], v195, v195 op_sel_hi:[0,0,0]
	s_setprio 0
	s_setprio 1
	v_mfma_scale_f32_16x16x128_f8f6f4 v[38:41], v[154:161], v[178:185], v[38:41], v195, v195 op_sel_hi:[0,0,0]
	v_mfma_scale_f32_16x16x128_f8f6f4 v[216:219], v[146:153], v[162:169], v[62:65], v195, v195 op_sel_hi:[0,0,0]
	v_mfma_scale_f32_16x16x128_f8f6f4 v[162:165], v[154:161], v[162:169], v[58:61], v195, v195 op_sel_hi:[0,0,0]
	v_mfma_scale_f32_16x16x128_f8f6f4 v[166:169], v[146:153], v[170:177], v[54:57], v195, v195 op_sel_hi:[0,0,0]
	v_mfma_scale_f32_16x16x128_f8f6f4 v[170:173], v[154:161], v[170:177], v[14:17], v195, v195 op_sel_hi:[0,0,0]
	v_mfma_scale_f32_16x16x128_f8f6f4 v[174:177], v[146:153], v[178:185], v[10:13], v195, v195 op_sel_hi:[0,0,0]
	v_mfma_scale_f32_16x16x128_f8f6f4 v[178:181], v[146:153], v[186:193], v[30:33], v195, v195 op_sel_hi:[0,0,0]
	v_mfma_scale_f32_16x16x128_f8f6f4 v[182:185], v[154:161], v[186:193], v[22:25], v195, v195 op_sel_hi:[0,0,0]
	s_setprio 0
	s_barrier
	v_mov_b32_e32 v203, v197
	s_nop 1
	s_add_i32 s34, s88, s43
	s_mov_b32 m0, s34
	v_lshl_add_u64 v[10:11], s[62:63], 0, v[202:203]
	global_load_lds_dwordx4 v202, s[62:63]
	v_lshl_add_u64 v[10:11], v[10:11], 0, s[12:13]
	s_add_i32 m0, s34, 0x2000
	s_add_i32 s34, s89, s43
	global_load_lds_dwordx4 v[10:11], off
	s_mov_b32 m0, s34
	v_lshl_add_u64 v[10:11], s[62:63], 0, v[202:203]
	v_lshl_add_u64 v[12:13], v[10:11], 0, s[14:15]
	global_load_lds_dwordx4 v[12:13], off
	v_lshl_add_u64 v[10:11], v[10:11], 0, s[16:17]
	s_add_i32 m0, s34, 0x2000
	s_nop 0
	global_load_lds_dwordx4 v[10:11], off
	s_mov_b32 m0, s64
	v_lshl_add_u64 v[10:11], s[60:61], 0, v[196:197]
	global_load_lds_dwordx4 v196, s[60:61]
	v_lshl_add_u64 v[10:11], v[10:11], 0, s[12:13]
	s_mov_b32 m0, s65
	s_nop 0
	global_load_lds_dwordx4 v[10:11], off
	v_add_u32_e32 v74, s85, v1
	ds_read_b128 v[46:49], v74 offset:16384
	ds_read_b128 v[50:53], v74 offset:17408
	ds_read_b128 v[54:57], v74 offset:18432
	ds_read_b128 v[58:61], v74 offset:19456
	ds_read_b128 v[62:65], v74 offset:20480
	ds_read_b128 v[66:69], v74 offset:21504
	ds_read_b128 v[70:73], v74 offset:22528
	ds_read_b128 v[74:77], v74 offset:23552
	s_waitcnt vmcnt(8)
	s_waitcnt lgkmcnt(0)
	s_barrier
	s_setprio 1
	s_waitcnt lgkmcnt(0)
	v_mfma_scale_f32_16x16x128_f8f6f4 v[42:45], v[130:137], v[46:53], v[42:45], v195, v195 op_sel_hi:[0,0,0]
	v_mfma_scale_f32_16x16x128_f8f6f4 v[34:37], v[138:145], v[46:53], v[34:37], v195, v195 op_sel_hi:[0,0,0]
	v_mfma_scale_f32_16x16x128_f8f6f4 v[224:227], v[130:137], v[62:69], v[224:227], v195, v195 op_sel_hi:[0,0,0]
	v_mfma_scale_f32_16x16x128_f8f6f4 v[228:231], v[138:145], v[62:69], v[228:231], v195, v195 op_sel_hi:[0,0,0]
	v_mfma_scale_f32_16x16x128_f8f6f4 v[186:189], v[130:137], v[54:61], v[26:29], v195, v195 op_sel_hi:[0,0,0]
	v_mfma_scale_f32_16x16x128_f8f6f4 v[190:193], v[138:145], v[54:61], v[18:21], v195, v195 op_sel_hi:[0,0,0]
	v_mfma_scale_f32_16x16x128_f8f6f4 v[232:235], v[130:137], v[70:77], v[6:9], v195, v195 op_sel_hi:[0,0,0]
	v_mfma_scale_f32_16x16x128_f8f6f4 v[236:239], v[138:145], v[70:77], v[2:5], v195, v195 op_sel_hi:[0,0,0]
	s_setprio 0
	s_setprio 1
	v_mfma_scale_f32_16x16x128_f8f6f4 v[240:243], v[146:153], v[46:53], v[98:101], v195, v195 op_sel_hi:[0,0,0]
	v_mfma_scale_f32_16x16x128_f8f6f4 v[244:247], v[154:161], v[46:53], v[102:105], v195, v195 op_sel_hi:[0,0,0]
	v_mfma_scale_f32_16x16x128_f8f6f4 v[248:251], v[146:153], v[54:61], v[106:109], v195, v195 op_sel_hi:[0,0,0]
	v_mfma_scale_f32_16x16x128_f8f6f4 v[198:201], v[154:161], v[54:61], v[110:113], v195, v195 op_sel_hi:[0,0,0]
	v_mfma_scale_f32_16x16x128_f8f6f4 v[220:223], v[146:153], v[62:69], v[114:117], v195, v195 op_sel_hi:[0,0,0]
	v_mfma_scale_f32_16x16x128_f8f6f4 v[46:49], v[154:161], v[62:69], v[118:121], v195, v195 op_sel_hi:[0,0,0]
	v_mfma_scale_f32_16x16x128_f8f6f4 v[50:53], v[146:153], v[70:77], v[122:125], v195, v195 op_sel_hi:[0,0,0]
	v_mfma_scale_f32_16x16x128_f8f6f4 v[154:157], v[154:161], v[70:77], v[126:129], v195, v195 op_sel_hi:[0,0,0]
	s_setprio 0
	s_barrier
	s_mov_b32 m0, s66
	v_lshl_add_u64 v[54:55], s[60:61], 0, v[196:197]
	v_lshl_add_u64 v[56:57], v[54:55], 0, s[14:15]
	global_load_lds_dwordx4 v[56:57], off
	v_lshl_add_u64 v[54:55], v[54:55], 0, s[16:17]
	s_mov_b32 m0, s67
	s_nop 0
	global_load_lds_dwordx4 v[54:55], off
	s_add_i32 s34, 0, 0x18000
	v_add_u32_e32 v10, s84, v1
	s_add_i32 s35, 0, 0x1c000
	v_add_u32_e32 v102, s34, v10
	v_add_u32_e32 v10, s35, v10
	ds_read_b128 v[2:5], v102
	ds_read_b128 v[6:9], v102 offset:1024
	ds_read_b128 v[98:101], v102 offset:2048
	ds_read_b128 v[102:105], v102 offset:3072
	ds_read_b128 v[122:125], v10
	ds_read_b128 v[126:129], v10 offset:1024
	ds_read_b128 v[130:133], v10 offset:2048
	ds_read_b128 v[134:137], v10 offset:3072
	v_add_u32_e32 v110, s85, v1
	ds_read_b128 v[10:13], v110 offset:32768
	ds_read_b128 v[14:17], v110 offset:33792
	ds_read_b128 v[18:21], v110 offset:34816
	ds_read_b128 v[22:25], v110 offset:35840
	ds_read_b128 v[26:29], v110 offset:36864
	ds_read_b128 v[30:33], v110 offset:37888
	ds_read_b128 v[106:109], v110 offset:38912
	ds_read_b128 v[110:113], v110 offset:39936
	s_waitcnt vmcnt(8)
	s_waitcnt lgkmcnt(0)
	s_barrier
	s_setprio 1
	s_waitcnt lgkmcnt(0)
	v_mfma_scale_f32_16x16x128_f8f6f4 v[94:97], v[2:9], v[10:17], v[94:97], v195, v195 op_sel_hi:[0,0,0]
	v_mfma_scale_f32_16x16x128_f8f6f4 v[90:93], v[98:105], v[10:17], v[90:93], v195, v195 op_sel_hi:[0,0,0]
	v_mfma_scale_f32_16x16x128_f8f6f4 v[86:89], v[2:9], v[18:25], v[86:89], v195, v195 op_sel_hi:[0,0,0]
	v_mfma_scale_f32_16x16x128_f8f6f4 v[82:85], v[98:105], v[18:25], v[82:85], v195, v195 op_sel_hi:[0,0,0]
	v_mfma_scale_f32_16x16x128_f8f6f4 v[78:81], v[2:9], v[26:33], v[78:81], v195, v195 op_sel_hi:[0,0,0]
	v_mfma_scale_f32_16x16x128_f8f6f4 v[74:77], v[98:105], v[26:33], v[204:207], v195, v195 op_sel_hi:[0,0,0]
	v_mfma_scale_f32_16x16x128_f8f6f4 v[70:73], v[2:9], v[106:113], v[208:211], v195, v195 op_sel_hi:[0,0,0]
	v_mfma_scale_f32_16x16x128_f8f6f4 v[66:69], v[98:105], v[106:113], v[212:215], v195, v195 op_sel_hi:[0,0,0]
	s_setprio 0
	s_setprio 1
	v_mfma_scale_f32_16x16x128_f8f6f4 v[62:65], v[122:129], v[10:17], v[216:219], v195, v195 op_sel_hi:[0,0,0]
	v_mfma_scale_f32_16x16x128_f8f6f4 v[58:61], v[130:137], v[10:17], v[162:165], v195, v195 op_sel_hi:[0,0,0]
	v_mfma_scale_f32_16x16x128_f8f6f4 v[54:57], v[122:129], v[18:25], v[166:169], v195, v195 op_sel_hi:[0,0,0]
	v_mfma_scale_f32_16x16x128_f8f6f4 v[14:17], v[130:137], v[18:25], v[170:173], v195, v195 op_sel_hi:[0,0,0]
	v_mfma_scale_f32_16x16x128_f8f6f4 v[10:13], v[122:129], v[26:33], v[174:177], v195, v195 op_sel_hi:[0,0,0]
	v_mfma_scale_f32_16x16x128_f8f6f4 v[38:41], v[130:137], v[26:33], v[38:41], v195, v195 op_sel_hi:[0,0,0]
	v_mfma_scale_f32_16x16x128_f8f6f4 v[30:33], v[122:129], v[106:113], v[178:181], v195, v195 op_sel_hi:[0,0,0]
	v_mfma_scale_f32_16x16x128_f8f6f4 v[22:25], v[130:137], v[106:113], v[182:185], v195, v195 op_sel_hi:[0,0,0]
	s_setprio 0
	s_barrier
	s_add_i32 s34, s34, s43
	s_mov_b32 m0, s34
	v_lshl_add_u64 v[18:19], s[62:63], 0, v[202:203]
	v_lshl_add_u64 v[20:21], v[18:19], 0, s[24:25]
	global_load_lds_dwordx4 v[20:21], off
	v_lshl_add_u64 v[18:19], v[18:19], 0, s[26:27]
	s_add_i32 m0, s34, 0x2000
	s_add_i32 s34, s35, s43
	global_load_lds_dwordx4 v[18:19], off
	s_mov_b32 m0, s34
	v_lshl_add_u64 v[18:19], s[62:63], 0, v[202:203]
	v_lshl_add_u64 v[20:21], v[18:19], 0, s[28:29]
	global_load_lds_dwordx4 v[20:21], off
	v_lshl_add_u64 v[18:19], v[18:19], 0, s[30:31]
	s_add_i32 m0, s34, 0x2000
	s_nop 0
	global_load_lds_dwordx4 v[18:19], off
	s_mov_b32 m0, s82
	v_lshl_add_u64 v[18:19], s[60:61], 0, v[196:197]
	v_lshl_add_u64 v[20:21], v[18:19], 0, s[24:25]
	global_load_lds_dwordx4 v[20:21], off
	v_lshl_add_u64 v[18:19], v[18:19], 0, s[26:27]
	s_mov_b32 m0, s83
	s_nop 0
	global_load_lds_dwordx4 v[18:19], off
	v_add_u32_e32 v150, s85, v1
	ds_read_b128 v[106:109], v150 offset:49152
	ds_read_b128 v[110:113], v150 offset:50176
	ds_read_b128 v[114:117], v150 offset:51200
	ds_read_b128 v[118:121], v150 offset:52224
	ds_read_b128 v[138:141], v150 offset:53248
	ds_read_b128 v[142:145], v150 offset:54272
	ds_read_b128 v[146:149], v150 offset:55296
	ds_read_b128 v[150:153], v150 offset:56320
	s_waitcnt vmcnt(8)
	s_waitcnt lgkmcnt(0)
	s_barrier
	s_setprio 1
	s_waitcnt lgkmcnt(0)
	v_mfma_scale_f32_16x16x128_f8f6f4 v[42:45], v[2:9], v[106:113], v[42:45], v195, v195 op_sel_hi:[0,0,0]
	v_mfma_scale_f32_16x16x128_f8f6f4 v[34:37], v[98:105], v[106:113], v[34:37], v195, v195 op_sel_hi:[0,0,0]
	v_mfma_scale_f32_16x16x128_f8f6f4 v[26:29], v[2:9], v[114:121], v[186:189], v195, v195 op_sel_hi:[0,0,0]
	v_mfma_scale_f32_16x16x128_f8f6f4 v[18:21], v[98:105], v[114:121], v[190:193], v195, v195 op_sel_hi:[0,0,0]
	v_mfma_scale_f32_16x16x128_f8f6f4 v[224:227], v[2:9], v[138:145], v[224:227], v195, v195 op_sel_hi:[0,0,0]
	v_mfma_scale_f32_16x16x128_f8f6f4 v[228:231], v[98:105], v[138:145], v[228:231], v195, v195 op_sel_hi:[0,0,0]
	v_mfma_scale_f32_16x16x128_f8f6f4 v[6:9], v[2:9], v[146:153], v[232:235], v195, v195 op_sel_hi:[0,0,0]
	v_mfma_scale_f32_16x16x128_f8f6f4 v[2:5], v[98:105], v[146:153], v[236:239], v195, v195 op_sel_hi:[0,0,0]
	s_setprio 0
	s_setprio 1
	v_mfma_scale_f32_16x16x128_f8f6f4 v[98:101], v[122:129], v[106:113], v[240:243], v195, v195 op_sel_hi:[0,0,0]
	v_mfma_scale_f32_16x16x128_f8f6f4 v[102:105], v[130:137], v[106:113], v[244:247], v195, v195 op_sel_hi:[0,0,0]
	v_mfma_scale_f32_16x16x128_f8f6f4 v[106:109], v[122:129], v[114:121], v[248:251], v195, v195 op_sel_hi:[0,0,0]
	v_mfma_scale_f32_16x16x128_f8f6f4 v[110:113], v[130:137], v[114:121], v[198:201], v195, v195 op_sel_hi:[0,0,0]
	v_mfma_scale_f32_16x16x128_f8f6f4 v[114:117], v[122:129], v[138:145], v[220:223], v195, v195 op_sel_hi:[0,0,0]
	v_mfma_scale_f32_16x16x128_f8f6f4 v[118:121], v[130:137], v[138:145], v[46:49], v195, v195 op_sel_hi:[0,0,0]
	v_mfma_scale_f32_16x16x128_f8f6f4 v[122:125], v[122:129], v[146:153], v[50:53], v195, v195 op_sel_hi:[0,0,0]
	v_mfma_scale_f32_16x16x128_f8f6f4 v[126:129], v[130:137], v[146:153], v[154:157], v195, v195 op_sel_hi:[0,0,0]
	s_setprio 0
	s_barrier
	s_add_i32 s70, s70, 2
	s_add_u32 s58, s58, 0x100
	s_addc_u32 s59, s59, 0
	s_add_u32 s68, s68, 0x100
	s_addc_u32 s69, s69, 0
	s_cmp_gt_u32 s70, 5
	s_cbranch_scc0 .LBB0_977
	s_and_b64 vcc, exec, s[36:37]
	s_cbranch_vccz .LBB0_980
	s_barrier

.LBB0_1074:
	s_add_u32 s2, s54, 0xfffa0080
	s_addc_u32 s34, s55, -1
	s_cmp_eq_u32 s76, 12
	s_cselect_b32 s57, s38, s34
	s_cselect_b32 s56, s39, s2
	s_cselect_b32 s59, s41, s75
	s_cselect_b32 s58, s43, s74
	s_mov_b32 s34, 0xfffe0000
	s_mov_b32 s35, -1
	v_lshl_add_u64 v[154:155], s[54:55], 0, v[158:159]
	v_lshl_add_u64 v[154:155], v[154:155], 0, s[34:35]
	s_add_i32 m0, s51, 0xc000
	s_nop 0
	global_load_lds_dwordx4 v[154:155], off
	s_add_i32 m0, s51, 0xe000
	s_nop 0
	global_load_lds_dwordx4 v158, s[54:55]
	v_add_u32_e32 v146, s66, v1
	v_add_u32_e32 v142, s71, v146
	v_add_u32_e32 v176, s72, v146
	ds_read_b128 v[130:133], v142
	ds_read_b128 v[134:137], v142 offset:1024
	ds_read_b128 v[138:141], v142 offset:2048
	ds_read_b128 v[142:145], v142 offset:3072
	ds_read_b128 v[146:149], v176
	ds_read_b128 v[150:153], v176 offset:1024
	ds_read_b128 v[172:175], v176 offset:2048
	ds_read_b128 v[176:179], v176 offset:3072
	v_add_u32_e32 v216, s67, v1
	ds_read_b128 v[180:183], v216
	ds_read_b128 v[184:187], v216 offset:1024
	ds_read_b128 v[196:199], v216 offset:2048
	ds_read_b128 v[200:203], v216 offset:3072
	ds_read_b128 v[204:207], v216 offset:4096
	ds_read_b128 v[208:211], v216 offset:5120
	ds_read_b128 v[212:215], v216 offset:6144
	ds_read_b128 v[216:219], v216 offset:7168
	s_waitcnt vmcnt(8)
	s_waitcnt lgkmcnt(0)
	s_barrier
	s_setprio 1
	s_waitcnt lgkmcnt(0)
	v_mfma_scale_f32_16x16x128_f8f6f4 v[126:129], v[130:137], v[180:187], v[126:129], v170, v170 op_sel_hi:[0,0,0]
	v_mfma_scale_f32_16x16x128_f8f6f4 v[122:125], v[138:145], v[180:187], v[122:125], v170, v170 op_sel_hi:[0,0,0]
	v_mfma_scale_f32_16x16x128_f8f6f4 v[114:117], v[130:137], v[196:203], v[114:117], v170, v170 op_sel_hi:[0,0,0]
	v_mfma_scale_f32_16x16x128_f8f6f4 v[106:109], v[138:145], v[196:203], v[106:109], v170, v170 op_sel_hi:[0,0,0]
	v_mfma_scale_f32_16x16x128_f8f6f4 v[98:101], v[130:137], v[204:211], v[98:101], v170, v170 op_sel_hi:[0,0,0]
	v_mfma_scale_f32_16x16x128_f8f6f4 v[154:157], v[138:145], v[204:211], v[90:93], v170, v170 op_sel_hi:[0,0,0]
	v_mfma_scale_f32_16x16x128_f8f6f4 v[166:169], v[130:137], v[212:219], v[82:85], v170, v170 op_sel_hi:[0,0,0]
	v_mfma_scale_f32_16x16x128_f8f6f4 v[188:191], v[138:145], v[212:219], v[74:77], v170, v170 op_sel_hi:[0,0,0]
	s_setprio 0
	s_setprio 1
	v_mfma_scale_f32_16x16x128_f8f6f4 v[118:121], v[146:153], v[180:187], v[118:121], v170, v170 op_sel_hi:[0,0,0]
	v_mfma_scale_f32_16x16x128_f8f6f4 v[110:113], v[172:179], v[180:187], v[110:113], v170, v170 op_sel_hi:[0,0,0]
	v_mfma_scale_f32_16x16x128_f8f6f4 v[102:105], v[146:153], v[196:203], v[102:105], v170, v170 op_sel_hi:[0,0,0]
	v_mfma_scale_f32_16x16x128_f8f6f4 v[180:183], v[172:179], v[196:203], v[94:97], v170, v170 op_sel_hi:[0,0,0]
	v_mfma_scale_f32_16x16x128_f8f6f4 v[184:187], v[146:153], v[204:211], v[86:89], v170, v170 op_sel_hi:[0,0,0]
	v_mfma_scale_f32_16x16x128_f8f6f4 v[192:195], v[172:179], v[204:211], v[78:81], v170, v170 op_sel_hi:[0,0,0]
	v_mfma_scale_f32_16x16x128_f8f6f4 v[196:199], v[146:153], v[212:219], v[70:73], v170, v170 op_sel_hi:[0,0,0]
	v_mfma_scale_f32_16x16x128_f8f6f4 v[200:203], v[172:179], v[212:219], v[66:69], v170, v170 op_sel_hi:[0,0,0]
	s_setprio 0
	s_barrier
	v_mov_b32_e32 v165, v159
	v_add_u32_e32 v94, s67, v1
	s_add_i32 s2, s71, s37
	s_nop 1
	s_mov_b32 m0, s2
	v_lshl_add_u64 v[204:205], s[58:59], 0, v[164:165]
	global_load_lds_dwordx4 v164, s[58:59]
	v_lshl_add_u64 v[204:205], v[204:205], 0, s[12:13]
	s_add_i32 m0, s2, 0x2000
	s_add_i32 s2, s72, s37
	global_load_lds_dwordx4 v[204:205], off
	s_mov_b32 m0, s2
	v_lshl_add_u64 v[204:205], s[58:59], 0, v[164:165]
	v_lshl_add_u64 v[206:207], v[204:205], 0, s[14:15]
	global_load_lds_dwordx4 v[206:207], off
	v_lshl_add_u64 v[204:205], v[204:205], 0, s[16:17]
	s_add_i32 m0, s2, 0x2000
	s_nop 0
	global_load_lds_dwordx4 v[204:205], off
	s_mov_b32 m0, s51
	v_lshl_add_u64 v[204:205], s[56:57], 0, v[158:159]
	global_load_lds_dwordx4 v158, s[56:57]
	v_lshl_add_u64 v[204:205], v[204:205], 0, s[12:13]
	s_mov_b32 m0, s60
	s_nop 0
	global_load_lds_dwordx4 v[204:205], off
	ds_read_b128 v[66:69], v94 offset:16384
	ds_read_b128 v[70:73], v94 offset:17408
	ds_read_b128 v[74:77], v94 offset:18432
	ds_read_b128 v[78:81], v94 offset:19456
	ds_read_b128 v[82:85], v94 offset:20480
	ds_read_b128 v[86:89], v94 offset:21504
	ds_read_b128 v[90:93], v94 offset:22528
	ds_read_b128 v[94:97], v94 offset:23552
	s_waitcnt vmcnt(8)
	s_waitcnt lgkmcnt(0)
	s_barrier
	s_setprio 1
	s_waitcnt lgkmcnt(0)
	v_mfma_scale_f32_16x16x128_f8f6f4 v[54:57], v[130:137], v[66:73], v[54:57], v170, v170 op_sel_hi:[0,0,0]
	v_mfma_scale_f32_16x16x128_f8f6f4 v[18:21], v[130:137], v[82:89], v[18:21], v170, v170 op_sel_hi:[0,0,0]
	v_mfma_scale_f32_16x16x128_f8f6f4 v[204:207], v[138:145], v[66:73], v[50:53], v170, v170 op_sel_hi:[0,0,0]
	v_mfma_scale_f32_16x16x128_f8f6f4 v[208:211], v[130:137], v[74:81], v[38:41], v170, v170 op_sel_hi:[0,0,0]
	v_mfma_scale_f32_16x16x128_f8f6f4 v[212:215], v[138:145], v[74:81], v[30:33], v170, v170 op_sel_hi:[0,0,0]
	v_mfma_scale_f32_16x16x128_f8f6f4 v[216:219], v[138:145], v[82:89], v[10:13], v170, v170 op_sel_hi:[0,0,0]
	v_mfma_scale_f32_16x16x128_f8f6f4 v[220:223], v[130:137], v[90:97], v[6:9], v170, v170 op_sel_hi:[0,0,0]
	v_mfma_scale_f32_16x16x128_f8f6f4 v[224:227], v[138:145], v[90:97], v[2:5], v170, v170 op_sel_hi:[0,0,0]
	s_setprio 0
	s_setprio 1
	v_mfma_scale_f32_16x16x128_f8f6f4 v[62:65], v[146:153], v[66:73], v[62:65], v170, v170 op_sel_hi:[0,0,0]
	v_mfma_scale_f32_16x16x128_f8f6f4 v[58:61], v[172:179], v[66:73], v[58:61], v170, v170 op_sel_hi:[0,0,0]
	v_mfma_scale_f32_16x16x128_f8f6f4 v[228:231], v[146:153], v[74:81], v[46:49], v170, v170 op_sel_hi:[0,0,0]
	v_mfma_scale_f32_16x16x128_f8f6f4 v[232:235], v[172:179], v[74:81], v[42:45], v170, v170 op_sel_hi:[0,0,0]
	v_mfma_scale_f32_16x16x128_f8f6f4 v[236:239], v[146:153], v[82:89], v[34:37], v170, v170 op_sel_hi:[0,0,0]
	v_mfma_scale_f32_16x16x128_f8f6f4 v[240:243], v[172:179], v[82:89], v[26:29], v170, v170 op_sel_hi:[0,0,0]
	v_mfma_scale_f32_16x16x128_f8f6f4 v[244:247], v[146:153], v[90:97], v[22:25], v170, v170 op_sel_hi:[0,0,0]
	v_mfma_scale_f32_16x16x128_f8f6f4 v[248:251], v[172:179], v[90:97], v[14:17], v170, v170 op_sel_hi:[0,0,0]
	s_setprio 0
	s_barrier
	s_mov_b32 m0, s61
	v_lshl_add_u64 v[66:67], s[56:57], 0, v[158:159]
	v_lshl_add_u64 v[68:69], v[66:67], 0, s[14:15]
	global_load_lds_dwordx4 v[68:69], off
	v_lshl_add_u64 v[66:67], v[66:67], 0, s[16:17]
	s_mov_b32 m0, s62
	s_nop 0
	global_load_lds_dwordx4 v[66:67], off
	s_add_i32 s2, 0, 0x18000
	v_add_u32_e32 v10, s66, v1
	s_add_i32 s34, 0, 0x1c000
	v_add_u32_e32 v26, s2, v10
	v_add_u32_e32 v10, s34, v10
	ds_read_b128 v[2:5], v26
	ds_read_b128 v[6:9], v26 offset:1024
	ds_read_b128 v[22:25], v26 offset:2048
	ds_read_b128 v[26:29], v26 offset:3072
	ds_read_b128 v[130:133], v10
	ds_read_b128 v[134:137], v10 offset:1024
	ds_read_b128 v[138:141], v10 offset:2048
	ds_read_b128 v[142:145], v10 offset:3072
	v_add_u32_e32 v50, s67, v1
	ds_read_b128 v[10:13], v50 offset:32768
	ds_read_b128 v[14:17], v50 offset:33792
	ds_read_b128 v[30:33], v50 offset:34816
	ds_read_b128 v[34:37], v50 offset:35840
	ds_read_b128 v[38:41], v50 offset:36864
	ds_read_b128 v[42:45], v50 offset:37888
	ds_read_b128 v[46:49], v50 offset:38912
	ds_read_b128 v[50:53], v50 offset:39936
	s_waitcnt vmcnt(8)
	s_waitcnt lgkmcnt(0)
	s_barrier
	s_setprio 1
	s_waitcnt lgkmcnt(0)
	v_mfma_scale_f32_16x16x128_f8f6f4 v[126:129], v[2:9], v[10:17], v[126:129], v170, v170 op_sel_hi:[0,0,0]
	v_mfma_scale_f32_16x16x128_f8f6f4 v[122:125], v[22:29], v[10:17], v[122:125], v170, v170 op_sel_hi:[0,0,0]
	v_mfma_scale_f32_16x16x128_f8f6f4 v[114:117], v[2:9], v[30:37], v[114:117], v170, v170 op_sel_hi:[0,0,0]
	v_mfma_scale_f32_16x16x128_f8f6f4 v[106:109], v[22:29], v[30:37], v[106:109], v170, v170 op_sel_hi:[0,0,0]
	v_mfma_scale_f32_16x16x128_f8f6f4 v[98:101], v[2:9], v[38:45], v[98:101], v170, v170 op_sel_hi:[0,0,0]
	v_mfma_scale_f32_16x16x128_f8f6f4 v[90:93], v[22:29], v[38:45], v[154:157], v170, v170 op_sel_hi:[0,0,0]
	v_mfma_scale_f32_16x16x128_f8f6f4 v[82:85], v[2:9], v[46:53], v[166:169], v170, v170 op_sel_hi:[0,0,0]
	v_mfma_scale_f32_16x16x128_f8f6f4 v[74:77], v[22:29], v[46:53], v[188:191], v170, v170 op_sel_hi:[0,0,0]
	s_setprio 0
	s_setprio 1
	v_mfma_scale_f32_16x16x128_f8f6f4 v[118:121], v[130:137], v[10:17], v[118:121], v170, v170 op_sel_hi:[0,0,0]
	v_mfma_scale_f32_16x16x128_f8f6f4 v[110:113], v[138:145], v[10:17], v[110:113], v170, v170 op_sel_hi:[0,0,0]
	v_mfma_scale_f32_16x16x128_f8f6f4 v[102:105], v[130:137], v[30:37], v[102:105], v170, v170 op_sel_hi:[0,0,0]
	v_mfma_scale_f32_16x16x128_f8f6f4 v[94:97], v[138:145], v[30:37], v[180:183], v170, v170 op_sel_hi:[0,0,0]
	v_mfma_scale_f32_16x16x128_f8f6f4 v[86:89], v[130:137], v[38:45], v[184:187], v170, v170 op_sel_hi:[0,0,0]
	v_mfma_scale_f32_16x16x128_f8f6f4 v[78:81], v[138:145], v[38:45], v[192:195], v170, v170 op_sel_hi:[0,0,0]
	v_mfma_scale_f32_16x16x128_f8f6f4 v[70:73], v[130:137], v[46:53], v[196:199], v170, v170 op_sel_hi:[0,0,0]
	v_mfma_scale_f32_16x16x128_f8f6f4 v[66:69], v[138:145], v[46:53], v[200:203], v170, v170 op_sel_hi:[0,0,0]
	s_setprio 0
	s_barrier
	s_add_i32 s2, s2, s37
	s_mov_b32 m0, s2
	v_lshl_add_u64 v[10:11], s[58:59], 0, v[164:165]
	v_lshl_add_u64 v[12:13], v[10:11], 0, s[22:23]
	global_load_lds_dwordx4 v[12:13], off
	v_lshl_add_u64 v[10:11], v[10:11], 0, s[24:25]
	s_add_i32 m0, s2, 0x2000
	s_add_i32 s2, s34, s37
	global_load_lds_dwordx4 v[10:11], off
	s_mov_b32 m0, s2
	v_lshl_add_u64 v[10:11], s[58:59], 0, v[164:165]
	v_lshl_add_u64 v[12:13], v[10:11], 0, s[26:27]
	global_load_lds_dwordx4 v[12:13], off
	v_lshl_add_u64 v[10:11], v[10:11], 0, s[28:29]
	s_add_i32 m0, s2, 0x2000
	s_nop 0
	global_load_lds_dwordx4 v[10:11], off
	s_mov_b32 m0, s64
	v_lshl_add_u64 v[10:11], s[56:57], 0, v[158:159]
	v_lshl_add_u64 v[12:13], v[10:11], 0, s[22:23]
	global_load_lds_dwordx4 v[12:13], off
	v_lshl_add_u64 v[10:11], v[10:11], 0, s[24:25]
	s_mov_b32 m0, s65
	s_nop 0
	global_load_lds_dwordx4 v[10:11], off
	v_add_u32_e32 v184, s67, v1
	ds_read_b128 v[42:45], v184 offset:49152
	ds_read_b128 v[46:49], v184 offset:50176
	ds_read_b128 v[146:149], v184 offset:51200
	ds_read_b128 v[150:153], v184 offset:52224
	ds_read_b128 v[172:175], v184 offset:53248
	ds_read_b128 v[176:179], v184 offset:54272
	ds_read_b128 v[180:183], v184 offset:55296
	ds_read_b128 v[184:187], v184 offset:56320
	s_waitcnt vmcnt(8)
	s_waitcnt lgkmcnt(0)
	s_barrier
	s_setprio 1
	s_waitcnt lgkmcnt(0)
	v_mfma_scale_f32_16x16x128_f8f6f4 v[54:57], v[2:9], v[42:49], v[54:57], v170, v170 op_sel_hi:[0,0,0]
	v_mfma_scale_f32_16x16x128_f8f6f4 v[50:53], v[22:29], v[42:49], v[204:207], v170, v170 op_sel_hi:[0,0,0]
	v_mfma_scale_f32_16x16x128_f8f6f4 v[38:41], v[2:9], v[146:153], v[208:211], v170, v170 op_sel_hi:[0,0,0]
	v_mfma_scale_f32_16x16x128_f8f6f4 v[30:33], v[22:29], v[146:153], v[212:215], v170, v170 op_sel_hi:[0,0,0]
	v_mfma_scale_f32_16x16x128_f8f6f4 v[18:21], v[2:9], v[172:179], v[18:21], v170, v170 op_sel_hi:[0,0,0]
	v_mfma_scale_f32_16x16x128_f8f6f4 v[10:13], v[22:29], v[172:179], v[216:219], v170, v170 op_sel_hi:[0,0,0]
	v_mfma_scale_f32_16x16x128_f8f6f4 v[6:9], v[2:9], v[180:187], v[220:223], v170, v170 op_sel_hi:[0,0,0]
	v_mfma_scale_f32_16x16x128_f8f6f4 v[2:5], v[22:29], v[180:187], v[224:227], v170, v170 op_sel_hi:[0,0,0]
	s_setprio 0
	s_setprio 1
	v_mfma_scale_f32_16x16x128_f8f6f4 v[62:65], v[130:137], v[42:49], v[62:65], v170, v170 op_sel_hi:[0,0,0]
	v_mfma_scale_f32_16x16x128_f8f6f4 v[58:61], v[138:145], v[42:49], v[58:61], v170, v170 op_sel_hi:[0,0,0]
	v_mfma_scale_f32_16x16x128_f8f6f4 v[46:49], v[130:137], v[146:153], v[228:231], v170, v170 op_sel_hi:[0,0,0]
	v_mfma_scale_f32_16x16x128_f8f6f4 v[42:45], v[138:145], v[146:153], v[232:235], v170, v170 op_sel_hi:[0,0,0]
	v_mfma_scale_f32_16x16x128_f8f6f4 v[34:37], v[130:137], v[172:179], v[236:239], v170, v170 op_sel_hi:[0,0,0]
	v_mfma_scale_f32_16x16x128_f8f6f4 v[26:29], v[138:145], v[172:179], v[240:243], v170, v170 op_sel_hi:[0,0,0]
	v_mfma_scale_f32_16x16x128_f8f6f4 v[22:25], v[130:137], v[180:187], v[244:247], v170, v170 op_sel_hi:[0,0,0]
	v_mfma_scale_f32_16x16x128_f8f6f4 v[14:17], v[138:145], v[180:187], v[248:251], v170, v170 op_sel_hi:[0,0,0]
	s_setprio 0
	s_barrier
	s_add_i32 s76, s76, 2
	s_add_u32 s54, s54, 0x100
	s_addc_u32 s55, s55, 0
	s_add_u32 s74, s74, 0x100
	s_addc_u32 s75, s75, 0
	s_cmp_gt_u32 s76, 13
	s_cbranch_scc0 .LBB0_1074
	s_and_b64 vcc, exec, s[30:31]
	s_cbranch_vccz .LBB0_1077
	s_barrier

.LBB0_1224:
	s_add_u32 s64, s46, s58
	v_add_u32_e32 v42, s76, v1
	v_add_u32_e32 v152, s79, v42
	v_add_u32_e32 v42, s81, v42
	ds_read_b128 v[140:143], v152
	ds_read_b128 v[144:147], v152 offset:1024
	ds_read_b128 v[148:151], v152 offset:2048
	ds_read_b128 v[152:155], v152 offset:3072
	ds_read_b128 v[156:159], v42
	ds_read_b128 v[160:163], v42 offset:1024
	ds_read_b128 v[164:167], v42 offset:2048
	ds_read_b128 v[168:171], v42 offset:3072
	s_addc_u32 s65, s47, s59
	s_add_u32 s34, s64, 0x100
	s_addc_u32 s35, s65, 0
	s_add_u32 s62, s2, s58
	s_addc_u32 s63, s49, s59
	s_cmpk_eq_i32 s58, 0x700
	s_cselect_b32 s61, s55, s35
	s_cselect_b32 s60, s54, s34
	s_cselect_b32 s63, s57, s63
	s_cselect_b32 s62, s56, s62
	s_add_i32 m0, s27, 0xc000
	v_lshl_add_u64 v[42:43], s[64:65], 0, v[130:131]
	v_lshl_add_u64 v[44:45], v[42:43], 0, s[38:39]
	global_load_lds_dwordx4 v[44:45], off
	v_lshl_add_u64 v[42:43], v[42:43], 0, s[40:41]
	s_add_i32 m0, s27, 0xe000
	s_nop 0
	global_load_lds_dwordx4 v[42:43], off
	v_add_u32_e32 v208, s77, v1
	v_mov_b64_e32 v[46:47], v[172:173]
	v_mov_b64_e32 v[50:51], v[176:177]
	v_mov_b64_e32 v[48:49], v[174:175]
	ds_read_b128 v[172:175], v208
	v_mov_b64_e32 v[52:53], v[178:179]
	ds_read_b128 v[176:179], v208 offset:1024
	ds_read_b128 v[180:183], v208 offset:2048
	ds_read_b128 v[184:187], v208 offset:3072
	ds_read_b128 v[196:199], v208 offset:4096
	ds_read_b128 v[200:203], v208 offset:5120
	ds_read_b128 v[204:207], v208 offset:6144
	ds_read_b128 v[208:211], v208 offset:7168
	s_waitcnt vmcnt(8)
	s_waitcnt lgkmcnt(0)
	s_barrier
	s_setprio 1
	s_waitcnt lgkmcnt(0)
	v_mfma_scale_f32_16x16x128_f8f6f4 v[94:97], v[140:147], v[172:179], v[94:97], v138, v138 op_sel_hi:[0,0,0]
	v_mfma_scale_f32_16x16x128_f8f6f4 v[90:93], v[148:155], v[172:179], v[90:93], v138, v138 op_sel_hi:[0,0,0]
	v_mfma_scale_f32_16x16x128_f8f6f4 v[86:89], v[140:147], v[180:187], v[86:89], v138, v138 op_sel_hi:[0,0,0]
	v_mfma_scale_f32_16x16x128_f8f6f4 v[82:85], v[148:155], v[180:187], v[82:85], v138, v138 op_sel_hi:[0,0,0]
	v_mfma_scale_f32_16x16x128_f8f6f4 v[78:81], v[140:147], v[196:203], v[78:81], v138, v138 op_sel_hi:[0,0,0]
	v_mfma_scale_f32_16x16x128_f8f6f4 v[74:77], v[148:155], v[196:203], v[74:77], v138, v138 op_sel_hi:[0,0,0]
	v_mfma_scale_f32_16x16x128_f8f6f4 v[134:137], v[140:147], v[204:211], v[70:73], v138, v138 op_sel_hi:[0,0,0]
	v_mfma_scale_f32_16x16x128_f8f6f4 v[188:191], v[148:155], v[204:211], v[66:69], v138, v138 op_sel_hi:[0,0,0]
	s_setprio 0
	s_setprio 1
	v_mfma_scale_f32_16x16x128_f8f6f4 v[192:195], v[156:163], v[172:179], v[62:65], v138, v138 op_sel_hi:[0,0,0]
	v_mfma_scale_f32_16x16x128_f8f6f4 v[172:175], v[164:171], v[172:179], v[58:61], v138, v138 op_sel_hi:[0,0,0]
	v_mfma_scale_f32_16x16x128_f8f6f4 v[176:179], v[156:163], v[180:187], v[54:57], v138, v138 op_sel_hi:[0,0,0]
	v_mfma_scale_f32_16x16x128_f8f6f4 v[180:183], v[164:171], v[180:187], v[50:53], v138, v138 op_sel_hi:[0,0,0]
	v_mfma_scale_f32_16x16x128_f8f6f4 v[184:187], v[156:163], v[196:203], v[46:49], v138, v138 op_sel_hi:[0,0,0]
	v_mfma_scale_f32_16x16x128_f8f6f4 v[196:199], v[164:171], v[196:203], v[18:21], v138, v138 op_sel_hi:[0,0,0]
	v_mfma_scale_f32_16x16x128_f8f6f4 v[200:203], v[156:163], v[204:211], v[6:9], v138, v138 op_sel_hi:[0,0,0]
	v_mfma_scale_f32_16x16x128_f8f6f4 v[204:207], v[164:171], v[204:211], v[14:17], v138, v138 op_sel_hi:[0,0,0]
	s_setprio 0
	s_barrier
	v_mov_b32_e32 v133, v131
	s_nop 2
	s_add_i32 s34, s79, s3
	s_mov_b32 m0, s34
	v_lshl_add_u64 v[6:7], s[62:63], 0, v[132:133]
	global_load_lds_dwordx4 v132, s[62:63]
	v_lshl_add_u64 v[6:7], v[6:7], 0, s[20:21]
	s_add_i32 m0, s34, 0x2000
	s_add_i32 s34, s81, s3
	global_load_lds_dwordx4 v[6:7], off
	s_mov_b32 m0, s34
	v_lshl_add_u64 v[6:7], s[62:63], 0, v[132:133]
	v_lshl_add_u64 v[8:9], v[6:7], 0, s[22:23]
	global_load_lds_dwordx4 v[8:9], off
	v_lshl_add_u64 v[6:7], v[6:7], 0, s[24:25]
	s_add_i32 m0, s34, 0x2000
	s_nop 0
	global_load_lds_dwordx4 v[6:7], off
	s_mov_b32 m0, s27
	v_lshl_add_u64 v[6:7], s[60:61], 0, v[130:131]
	global_load_lds_dwordx4 v130, s[60:61]
	v_lshl_add_u64 v[6:7], v[6:7], 0, s[20:21]
	s_mov_b32 m0, s70
	s_nop 0
	global_load_lds_dwordx4 v[6:7], off
	v_add_u32_e32 v70, s77, v1
	ds_read_b128 v[42:45], v70 offset:16384
	ds_read_b128 v[46:49], v70 offset:17408
	ds_read_b128 v[50:53], v70 offset:18432
	ds_read_b128 v[54:57], v70 offset:19456
	ds_read_b128 v[58:61], v70 offset:20480
	ds_read_b128 v[62:65], v70 offset:21504
	ds_read_b128 v[66:69], v70 offset:22528
	ds_read_b128 v[70:73], v70 offset:23552
	s_waitcnt vmcnt(8)
	s_waitcnt lgkmcnt(0)
	s_barrier
	s_setprio 1
	s_waitcnt lgkmcnt(0)
	v_mfma_scale_f32_16x16x128_f8f6f4 v[38:41], v[140:147], v[42:49], v[38:41], v138, v138 op_sel_hi:[0,0,0]
	v_mfma_scale_f32_16x16x128_f8f6f4 v[34:37], v[148:155], v[42:49], v[34:37], v138, v138 op_sel_hi:[0,0,0]
	v_mfma_scale_f32_16x16x128_f8f6f4 v[220:223], v[148:155], v[58:65], v[220:223], v138, v138 op_sel_hi:[0,0,0]
	v_mfma_scale_f32_16x16x128_f8f6f4 v[208:211], v[140:147], v[50:57], v[30:33], v138, v138 op_sel_hi:[0,0,0]
	v_mfma_scale_f32_16x16x128_f8f6f4 v[212:215], v[148:155], v[50:57], v[26:29], v138, v138 op_sel_hi:[0,0,0]
	v_mfma_scale_f32_16x16x128_f8f6f4 v[216:219], v[140:147], v[58:65], v[22:25], v138, v138 op_sel_hi:[0,0,0]
	v_mfma_scale_f32_16x16x128_f8f6f4 v[224:227], v[140:147], v[66:73], v[2:5], v138, v138 op_sel_hi:[0,0,0]
	v_mfma_scale_f32_16x16x128_f8f6f4 v[228:231], v[148:155], v[66:73], v[10:13], v138, v138 op_sel_hi:[0,0,0]
	s_setprio 0
	s_setprio 1
	v_mfma_scale_f32_16x16x128_f8f6f4 v[232:235], v[156:163], v[42:49], v[98:101], v138, v138 op_sel_hi:[0,0,0]
	v_mfma_scale_f32_16x16x128_f8f6f4 v[236:239], v[164:171], v[42:49], v[102:105], v138, v138 op_sel_hi:[0,0,0]
	v_mfma_scale_f32_16x16x128_f8f6f4 v[240:243], v[156:163], v[50:57], v[106:109], v138, v138 op_sel_hi:[0,0,0]
	v_mfma_scale_f32_16x16x128_f8f6f4 v[244:247], v[164:171], v[50:57], v[110:113], v138, v138 op_sel_hi:[0,0,0]
	v_mfma_scale_f32_16x16x128_f8f6f4 v[248:251], v[156:163], v[58:65], v[114:117], v138, v138 op_sel_hi:[0,0,0]
	v_mfma_scale_f32_16x16x128_f8f6f4 v[42:45], v[164:171], v[58:65], v[118:121], v138, v138 op_sel_hi:[0,0,0]
	v_mfma_scale_f32_16x16x128_f8f6f4 v[46:49], v[156:163], v[66:73], v[122:125], v138, v138 op_sel_hi:[0,0,0]
	v_mfma_scale_f32_16x16x128_f8f6f4 v[50:53], v[164:171], v[66:73], v[126:129], v138, v138 op_sel_hi:[0,0,0]
	s_setprio 0
	s_barrier
	s_mov_b32 m0, s71
	v_lshl_add_u64 v[54:55], s[60:61], 0, v[130:131]
	v_lshl_add_u64 v[56:57], v[54:55], 0, s[22:23]
	global_load_lds_dwordx4 v[56:57], off
	v_lshl_add_u64 v[54:55], v[54:55], 0, s[24:25]
	s_mov_b32 m0, s72
	s_nop 0
	global_load_lds_dwordx4 v[54:55], off
	s_add_i32 s34, 0, 0x18000
	v_add_u32_e32 v2, s76, v1
	s_add_i32 s35, 0, 0x1c000
	v_add_u32_e32 v110, s34, v2
	v_add_u32_e32 v2, s35, v2
	ds_read_b128 v[98:101], v110
	ds_read_b128 v[102:105], v110 offset:1024
	ds_read_b128 v[106:109], v110 offset:2048
	ds_read_b128 v[110:113], v110 offset:3072
	ds_read_b128 v[122:125], v2
	ds_read_b128 v[126:129], v2 offset:1024
	ds_read_b128 v[140:143], v2 offset:2048
	ds_read_b128 v[144:147], v2 offset:3072
	v_add_u32_e32 v30, s77, v1
	ds_read_b128 v[2:5], v30 offset:32768
	ds_read_b128 v[6:9], v30 offset:33792
	ds_read_b128 v[10:13], v30 offset:34816
	ds_read_b128 v[14:17], v30 offset:35840
	ds_read_b128 v[18:21], v30 offset:36864
	ds_read_b128 v[22:25], v30 offset:37888
	ds_read_b128 v[26:29], v30 offset:38912
	ds_read_b128 v[30:33], v30 offset:39936
	s_waitcnt vmcnt(8)
	s_waitcnt lgkmcnt(0)
	s_barrier
	s_setprio 1
	s_waitcnt lgkmcnt(0)
	v_mfma_scale_f32_16x16x128_f8f6f4 v[94:97], v[98:105], v[2:9], v[94:97], v138, v138 op_sel_hi:[0,0,0]
	v_mfma_scale_f32_16x16x128_f8f6f4 v[90:93], v[106:113], v[2:9], v[90:93], v138, v138 op_sel_hi:[0,0,0]
	v_mfma_scale_f32_16x16x128_f8f6f4 v[86:89], v[98:105], v[10:17], v[86:89], v138, v138 op_sel_hi:[0,0,0]
	v_mfma_scale_f32_16x16x128_f8f6f4 v[82:85], v[106:113], v[10:17], v[82:85], v138, v138 op_sel_hi:[0,0,0]
	v_mfma_scale_f32_16x16x128_f8f6f4 v[78:81], v[98:105], v[18:25], v[78:81], v138, v138 op_sel_hi:[0,0,0]
	v_mfma_scale_f32_16x16x128_f8f6f4 v[74:77], v[106:113], v[18:25], v[74:77], v138, v138 op_sel_hi:[0,0,0]
	v_mfma_scale_f32_16x16x128_f8f6f4 v[70:73], v[98:105], v[26:33], v[134:137], v138, v138 op_sel_hi:[0,0,0]
	v_mfma_scale_f32_16x16x128_f8f6f4 v[66:69], v[106:113], v[26:33], v[188:191], v138, v138 op_sel_hi:[0,0,0]
	s_setprio 0
	s_setprio 1
	v_mfma_scale_f32_16x16x128_f8f6f4 v[62:65], v[122:129], v[2:9], v[192:195], v138, v138 op_sel_hi:[0,0,0]
	v_mfma_scale_f32_16x16x128_f8f6f4 v[58:61], v[140:147], v[2:9], v[172:175], v138, v138 op_sel_hi:[0,0,0]
	v_mfma_scale_f32_16x16x128_f8f6f4 v[54:57], v[122:129], v[10:17], v[176:179], v138, v138 op_sel_hi:[0,0,0]
	v_mfma_scale_f32_16x16x128_f8f6f4 v[176:179], v[140:147], v[10:17], v[180:183], v138, v138 op_sel_hi:[0,0,0]
	v_mfma_scale_f32_16x16x128_f8f6f4 v[172:175], v[122:129], v[18:25], v[184:187], v138, v138 op_sel_hi:[0,0,0]
	v_mfma_scale_f32_16x16x128_f8f6f4 v[18:21], v[140:147], v[18:25], v[196:199], v138, v138 op_sel_hi:[0,0,0]
	v_mfma_scale_f32_16x16x128_f8f6f4 v[6:9], v[122:129], v[26:33], v[200:203], v138, v138 op_sel_hi:[0,0,0]
	v_mfma_scale_f32_16x16x128_f8f6f4 v[14:17], v[140:147], v[26:33], v[204:207], v138, v138 op_sel_hi:[0,0,0]
	s_setprio 0
	s_barrier
	s_add_i32 s34, s34, s3
	s_mov_b32 m0, s34
	v_lshl_add_u64 v[2:3], s[62:63], 0, v[132:133]
	v_lshl_add_u64 v[4:5], v[2:3], 0, s[30:31]
	global_load_lds_dwordx4 v[4:5], off
	v_lshl_add_u64 v[2:3], v[2:3], 0, s[36:37]
	s_add_i32 m0, s34, 0x2000
	s_add_i32 s34, s35, s3
	global_load_lds_dwordx4 v[2:3], off
	s_mov_b32 m0, s34
	v_lshl_add_u64 v[2:3], s[62:63], 0, v[132:133]
	v_lshl_add_u64 v[4:5], v[2:3], 0, s[38:39]
	global_load_lds_dwordx4 v[4:5], off
	v_lshl_add_u64 v[2:3], v[2:3], 0, s[40:41]
	s_add_i32 m0, s34, 0x2000
	s_nop 0
	global_load_lds_dwordx4 v[2:3], off
	s_mov_b32 m0, s73
	v_lshl_add_u64 v[2:3], s[60:61], 0, v[130:131]
	v_lshl_add_u64 v[4:5], v[2:3], 0, s[30:31]
	global_load_lds_dwordx4 v[4:5], off
	v_lshl_add_u64 v[2:3], v[2:3], 0, s[36:37]
	s_mov_b32 m0, s74
	s_nop 0
	global_load_lds_dwordx4 v[2:3], off
	v_add_u32_e32 v168, s77, v1
	ds_read_b128 v[114:117], v168 offset:49152
	ds_read_b128 v[118:121], v168 offset:50176
	ds_read_b128 v[148:151], v168 offset:51200
	ds_read_b128 v[152:155], v168 offset:52224
	ds_read_b128 v[156:159], v168 offset:53248
	ds_read_b128 v[160:163], v168 offset:54272
	ds_read_b128 v[164:167], v168 offset:55296
	ds_read_b128 v[168:171], v168 offset:56320
	s_waitcnt vmcnt(8)
	s_waitcnt lgkmcnt(0)
	s_barrier
	s_setprio 1
	s_waitcnt lgkmcnt(0)
	v_mfma_scale_f32_16x16x128_f8f6f4 v[38:41], v[98:105], v[114:121], v[38:41], v138, v138 op_sel_hi:[0,0,0]
	v_mfma_scale_f32_16x16x128_f8f6f4 v[34:37], v[106:113], v[114:121], v[34:37], v138, v138 op_sel_hi:[0,0,0]
	v_mfma_scale_f32_16x16x128_f8f6f4 v[30:33], v[98:105], v[148:155], v[208:211], v138, v138 op_sel_hi:[0,0,0]
	v_mfma_scale_f32_16x16x128_f8f6f4 v[26:29], v[106:113], v[148:155], v[212:215], v138, v138 op_sel_hi:[0,0,0]
	v_mfma_scale_f32_16x16x128_f8f6f4 v[22:25], v[98:105], v[156:163], v[216:219], v138, v138 op_sel_hi:[0,0,0]
	v_mfma_scale_f32_16x16x128_f8f6f4 v[220:223], v[106:113], v[156:163], v[220:223], v138, v138 op_sel_hi:[0,0,0]
	v_mfma_scale_f32_16x16x128_f8f6f4 v[2:5], v[98:105], v[164:171], v[224:227], v138, v138 op_sel_hi:[0,0,0]
	v_mfma_scale_f32_16x16x128_f8f6f4 v[10:13], v[106:113], v[164:171], v[228:231], v138, v138 op_sel_hi:[0,0,0]
	s_setprio 0
	s_setprio 1
	v_mfma_scale_f32_16x16x128_f8f6f4 v[98:101], v[122:129], v[114:121], v[232:235], v138, v138 op_sel_hi:[0,0,0]
	v_mfma_scale_f32_16x16x128_f8f6f4 v[102:105], v[140:147], v[114:121], v[236:239], v138, v138 op_sel_hi:[0,0,0]
	v_mfma_scale_f32_16x16x128_f8f6f4 v[106:109], v[122:129], v[148:155], v[240:243], v138, v138 op_sel_hi:[0,0,0]
	v_mfma_scale_f32_16x16x128_f8f6f4 v[110:113], v[140:147], v[148:155], v[244:247], v138, v138 op_sel_hi:[0,0,0]
	v_mfma_scale_f32_16x16x128_f8f6f4 v[114:117], v[122:129], v[156:163], v[248:251], v138, v138 op_sel_hi:[0,0,0]
	v_mfma_scale_f32_16x16x128_f8f6f4 v[118:121], v[140:147], v[156:163], v[42:45], v138, v138 op_sel_hi:[0,0,0]
	v_mfma_scale_f32_16x16x128_f8f6f4 v[122:125], v[122:129], v[164:171], v[46:49], v138, v138 op_sel_hi:[0,0,0]
	v_mfma_scale_f32_16x16x128_f8f6f4 v[126:129], v[140:147], v[164:171], v[50:53], v138, v138 op_sel_hi:[0,0,0]
	s_setprio 0
	s_barrier
	s_add_i32 s51, s51, 2
	s_add_u32 s58, s58, 0x100
	s_addc_u32 s59, s59, 0
	s_cmp_gt_u32 s51, 13
	s_cbranch_scc0 .LBB0_1224
	s_and_b64 vcc, exec, s[44:45]
	s_cbranch_vccz .LBB0_1227
	s_barrier

.LBB0_1257:
	s_add_u32 s60, s42, s54
	v_add_u32_e32 v42, s75, v1
	v_add_u32_e32 v152, s78, v42
	v_add_u32_e32 v42, s79, v42
	ds_read_b128 v[140:143], v152
	ds_read_b128 v[144:147], v152 offset:1024
	ds_read_b128 v[148:151], v152 offset:2048
	ds_read_b128 v[152:155], v152 offset:3072
	ds_read_b128 v[156:159], v42
	ds_read_b128 v[160:163], v42 offset:1024
	ds_read_b128 v[164:167], v42 offset:2048
	ds_read_b128 v[168:171], v42 offset:3072
	s_addc_u32 s61, s43, s55
	s_add_u32 s34, s60, 0x100
	s_addc_u32 s35, s61, 0
	s_add_u32 s58, s45, s54
	s_addc_u32 s59, s47, s55
	s_cmpk_eq_i32 s54, 0x700
	s_cselect_b32 s57, s51, s35
	s_cselect_b32 s56, s50, s34
	s_cselect_b32 s59, s53, s59
	s_cselect_b32 s58, s52, s58
	s_add_i32 m0, s23, 0xc000
	v_lshl_add_u64 v[42:43], s[60:61], 0, v[130:131]
	v_lshl_add_u64 v[44:45], v[42:43], 0, s[30:31]
	global_load_lds_dwordx4 v[44:45], off
	v_lshl_add_u64 v[42:43], v[42:43], 0, s[36:37]
	s_add_i32 m0, s23, 0xe000
	s_nop 0
	global_load_lds_dwordx4 v[42:43], off
	v_add_u32_e32 v208, s76, v1
	v_mov_b64_e32 v[46:47], v[172:173]
	v_mov_b64_e32 v[50:51], v[176:177]
	v_mov_b64_e32 v[48:49], v[174:175]
	ds_read_b128 v[172:175], v208
	v_mov_b64_e32 v[52:53], v[178:179]
	ds_read_b128 v[176:179], v208 offset:1024
	ds_read_b128 v[180:183], v208 offset:2048
	ds_read_b128 v[184:187], v208 offset:3072
	ds_read_b128 v[196:199], v208 offset:4096
	ds_read_b128 v[200:203], v208 offset:5120
	ds_read_b128 v[204:207], v208 offset:6144
	ds_read_b128 v[208:211], v208 offset:7168
	s_waitcnt vmcnt(8)
	s_waitcnt lgkmcnt(0)
	s_barrier
	s_setprio 1
	s_waitcnt lgkmcnt(0)
	v_mfma_scale_f32_16x16x128_f8f6f4 v[94:97], v[140:147], v[172:179], v[94:97], v138, v138 op_sel_hi:[0,0,0]
	v_mfma_scale_f32_16x16x128_f8f6f4 v[90:93], v[148:155], v[172:179], v[90:93], v138, v138 op_sel_hi:[0,0,0]
	v_mfma_scale_f32_16x16x128_f8f6f4 v[86:89], v[140:147], v[180:187], v[86:89], v138, v138 op_sel_hi:[0,0,0]
	v_mfma_scale_f32_16x16x128_f8f6f4 v[82:85], v[148:155], v[180:187], v[82:85], v138, v138 op_sel_hi:[0,0,0]
	v_mfma_scale_f32_16x16x128_f8f6f4 v[78:81], v[140:147], v[196:203], v[78:81], v138, v138 op_sel_hi:[0,0,0]
	v_mfma_scale_f32_16x16x128_f8f6f4 v[74:77], v[148:155], v[196:203], v[74:77], v138, v138 op_sel_hi:[0,0,0]
	v_mfma_scale_f32_16x16x128_f8f6f4 v[134:137], v[140:147], v[204:211], v[70:73], v138, v138 op_sel_hi:[0,0,0]
	v_mfma_scale_f32_16x16x128_f8f6f4 v[188:191], v[148:155], v[204:211], v[66:69], v138, v138 op_sel_hi:[0,0,0]
	s_setprio 0
	s_setprio 1
	v_mfma_scale_f32_16x16x128_f8f6f4 v[192:195], v[156:163], v[172:179], v[62:65], v138, v138 op_sel_hi:[0,0,0]
	v_mfma_scale_f32_16x16x128_f8f6f4 v[172:175], v[164:171], v[172:179], v[58:61], v138, v138 op_sel_hi:[0,0,0]
	v_mfma_scale_f32_16x16x128_f8f6f4 v[176:179], v[156:163], v[180:187], v[54:57], v138, v138 op_sel_hi:[0,0,0]
	v_mfma_scale_f32_16x16x128_f8f6f4 v[180:183], v[164:171], v[180:187], v[50:53], v138, v138 op_sel_hi:[0,0,0]
	v_mfma_scale_f32_16x16x128_f8f6f4 v[184:187], v[156:163], v[196:203], v[46:49], v138, v138 op_sel_hi:[0,0,0]
	v_mfma_scale_f32_16x16x128_f8f6f4 v[196:199], v[164:171], v[196:203], v[18:21], v138, v138 op_sel_hi:[0,0,0]
	v_mfma_scale_f32_16x16x128_f8f6f4 v[200:203], v[156:163], v[204:211], v[6:9], v138, v138 op_sel_hi:[0,0,0]
	v_mfma_scale_f32_16x16x128_f8f6f4 v[204:207], v[164:171], v[204:211], v[14:17], v138, v138 op_sel_hi:[0,0,0]
	s_setprio 0
	s_barrier
	v_mov_b32_e32 v133, v131
	s_nop 2
	s_add_i32 s34, s78, s39
	s_mov_b32 m0, s34
	v_lshl_add_u64 v[6:7], s[58:59], 0, v[132:133]
	global_load_lds_dwordx4 v132, s[58:59]
	v_lshl_add_u64 v[6:7], v[6:7], 0, s[8:9]
	s_add_i32 m0, s34, 0x2000
	s_add_i32 s34, s79, s39
	global_load_lds_dwordx4 v[6:7], off
	s_mov_b32 m0, s34
	v_lshl_add_u64 v[6:7], s[58:59], 0, v[132:133]
	v_lshl_add_u64 v[8:9], v[6:7], 0, s[18:19]
	global_load_lds_dwordx4 v[8:9], off
	v_lshl_add_u64 v[6:7], v[6:7], 0, s[20:21]
	s_add_i32 m0, s34, 0x2000
	s_nop 0
	global_load_lds_dwordx4 v[6:7], off
	s_mov_b32 m0, s23
	v_lshl_add_u64 v[6:7], s[56:57], 0, v[130:131]
	global_load_lds_dwordx4 v130, s[56:57]
	v_lshl_add_u64 v[6:7], v[6:7], 0, s[8:9]
	s_mov_b32 m0, s69
	s_nop 0
	global_load_lds_dwordx4 v[6:7], off
	v_add_u32_e32 v70, s76, v1
	ds_read_b128 v[42:45], v70 offset:16384
	ds_read_b128 v[46:49], v70 offset:17408
	ds_read_b128 v[50:53], v70 offset:18432
	ds_read_b128 v[54:57], v70 offset:19456
	ds_read_b128 v[58:61], v70 offset:20480
	ds_read_b128 v[62:65], v70 offset:21504
	ds_read_b128 v[66:69], v70 offset:22528
	ds_read_b128 v[70:73], v70 offset:23552
	s_waitcnt vmcnt(8)
	s_waitcnt lgkmcnt(0)
	s_barrier
	s_setprio 1
	s_waitcnt lgkmcnt(0)
	v_mfma_scale_f32_16x16x128_f8f6f4 v[38:41], v[140:147], v[42:49], v[38:41], v138, v138 op_sel_hi:[0,0,0]
	v_mfma_scale_f32_16x16x128_f8f6f4 v[34:37], v[148:155], v[42:49], v[34:37], v138, v138 op_sel_hi:[0,0,0]
	v_mfma_scale_f32_16x16x128_f8f6f4 v[220:223], v[148:155], v[58:65], v[220:223], v138, v138 op_sel_hi:[0,0,0]
	v_mfma_scale_f32_16x16x128_f8f6f4 v[208:211], v[140:147], v[50:57], v[30:33], v138, v138 op_sel_hi:[0,0,0]
	v_mfma_scale_f32_16x16x128_f8f6f4 v[212:215], v[148:155], v[50:57], v[26:29], v138, v138 op_sel_hi:[0,0,0]
	v_mfma_scale_f32_16x16x128_f8f6f4 v[216:219], v[140:147], v[58:65], v[22:25], v138, v138 op_sel_hi:[0,0,0]
	v_mfma_scale_f32_16x16x128_f8f6f4 v[224:227], v[140:147], v[66:73], v[2:5], v138, v138 op_sel_hi:[0,0,0]
	v_mfma_scale_f32_16x16x128_f8f6f4 v[228:231], v[148:155], v[66:73], v[10:13], v138, v138 op_sel_hi:[0,0,0]
	s_setprio 0
	s_setprio 1
	v_mfma_scale_f32_16x16x128_f8f6f4 v[232:235], v[156:163], v[42:49], v[98:101], v138, v138 op_sel_hi:[0,0,0]
	v_mfma_scale_f32_16x16x128_f8f6f4 v[236:239], v[164:171], v[42:49], v[102:105], v138, v138 op_sel_hi:[0,0,0]
	v_mfma_scale_f32_16x16x128_f8f6f4 v[240:243], v[156:163], v[50:57], v[106:109], v138, v138 op_sel_hi:[0,0,0]
	v_mfma_scale_f32_16x16x128_f8f6f4 v[244:247], v[164:171], v[50:57], v[110:113], v138, v138 op_sel_hi:[0,0,0]
	v_mfma_scale_f32_16x16x128_f8f6f4 v[248:251], v[156:163], v[58:65], v[114:117], v138, v138 op_sel_hi:[0,0,0]
	v_mfma_scale_f32_16x16x128_f8f6f4 v[42:45], v[164:171], v[58:65], v[118:121], v138, v138 op_sel_hi:[0,0,0]
	v_mfma_scale_f32_16x16x128_f8f6f4 v[46:49], v[156:163], v[66:73], v[122:125], v138, v138 op_sel_hi:[0,0,0]
	v_mfma_scale_f32_16x16x128_f8f6f4 v[50:53], v[164:171], v[66:73], v[126:129], v138, v138 op_sel_hi:[0,0,0]
	s_setprio 0
	s_barrier
	s_mov_b32 m0, s70
	v_lshl_add_u64 v[54:55], s[56:57], 0, v[130:131]
	v_lshl_add_u64 v[56:57], v[54:55], 0, s[18:19]
	global_load_lds_dwordx4 v[56:57], off
	v_lshl_add_u64 v[54:55], v[54:55], 0, s[20:21]
	s_mov_b32 m0, s71
	s_nop 0
	global_load_lds_dwordx4 v[54:55], off
	s_add_i32 s34, 0, 0x18000
	v_add_u32_e32 v2, s75, v1
	s_add_i32 s35, 0, 0x1c000
	v_add_u32_e32 v110, s34, v2
	v_add_u32_e32 v2, s35, v2
	ds_read_b128 v[98:101], v110
	ds_read_b128 v[102:105], v110 offset:1024
	ds_read_b128 v[106:109], v110 offset:2048
	ds_read_b128 v[110:113], v110 offset:3072
	ds_read_b128 v[122:125], v2
	ds_read_b128 v[126:129], v2 offset:1024
	ds_read_b128 v[140:143], v2 offset:2048
	ds_read_b128 v[144:147], v2 offset:3072
	v_add_u32_e32 v30, s76, v1
	ds_read_b128 v[2:5], v30 offset:32768
	ds_read_b128 v[6:9], v30 offset:33792
	ds_read_b128 v[10:13], v30 offset:34816
	ds_read_b128 v[14:17], v30 offset:35840
	ds_read_b128 v[18:21], v30 offset:36864
	ds_read_b128 v[22:25], v30 offset:37888
	ds_read_b128 v[26:29], v30 offset:38912
	ds_read_b128 v[30:33], v30 offset:39936
	s_waitcnt vmcnt(8)
	s_waitcnt lgkmcnt(0)
	s_barrier
	s_setprio 1
	s_waitcnt lgkmcnt(0)
	v_mfma_scale_f32_16x16x128_f8f6f4 v[94:97], v[98:105], v[2:9], v[94:97], v138, v138 op_sel_hi:[0,0,0]
	v_mfma_scale_f32_16x16x128_f8f6f4 v[90:93], v[106:113], v[2:9], v[90:93], v138, v138 op_sel_hi:[0,0,0]
	v_mfma_scale_f32_16x16x128_f8f6f4 v[86:89], v[98:105], v[10:17], v[86:89], v138, v138 op_sel_hi:[0,0,0]
	v_mfma_scale_f32_16x16x128_f8f6f4 v[82:85], v[106:113], v[10:17], v[82:85], v138, v138 op_sel_hi:[0,0,0]
	v_mfma_scale_f32_16x16x128_f8f6f4 v[78:81], v[98:105], v[18:25], v[78:81], v138, v138 op_sel_hi:[0,0,0]
	v_mfma_scale_f32_16x16x128_f8f6f4 v[74:77], v[106:113], v[18:25], v[74:77], v138, v138 op_sel_hi:[0,0,0]
	v_mfma_scale_f32_16x16x128_f8f6f4 v[70:73], v[98:105], v[26:33], v[134:137], v138, v138 op_sel_hi:[0,0,0]
	v_mfma_scale_f32_16x16x128_f8f6f4 v[66:69], v[106:113], v[26:33], v[188:191], v138, v138 op_sel_hi:[0,0,0]
	s_setprio 0
	s_setprio 1
	v_mfma_scale_f32_16x16x128_f8f6f4 v[62:65], v[122:129], v[2:9], v[192:195], v138, v138 op_sel_hi:[0,0,0]
	v_mfma_scale_f32_16x16x128_f8f6f4 v[58:61], v[140:147], v[2:9], v[172:175], v138, v138 op_sel_hi:[0,0,0]
	v_mfma_scale_f32_16x16x128_f8f6f4 v[54:57], v[122:129], v[10:17], v[176:179], v138, v138 op_sel_hi:[0,0,0]
	v_mfma_scale_f32_16x16x128_f8f6f4 v[176:179], v[140:147], v[10:17], v[180:183], v138, v138 op_sel_hi:[0,0,0]
	v_mfma_scale_f32_16x16x128_f8f6f4 v[172:175], v[122:129], v[18:25], v[184:187], v138, v138 op_sel_hi:[0,0,0]
	v_mfma_scale_f32_16x16x128_f8f6f4 v[18:21], v[140:147], v[18:25], v[196:199], v138, v138 op_sel_hi:[0,0,0]
	v_mfma_scale_f32_16x16x128_f8f6f4 v[6:9], v[122:129], v[26:33], v[200:203], v138, v138 op_sel_hi:[0,0,0]
	v_mfma_scale_f32_16x16x128_f8f6f4 v[14:17], v[140:147], v[26:33], v[204:207], v138, v138 op_sel_hi:[0,0,0]
	s_setprio 0
	s_barrier
	s_add_i32 s34, s34, s39
	s_mov_b32 m0, s34
	v_lshl_add_u64 v[2:3], s[58:59], 0, v[132:133]
	v_lshl_add_u64 v[4:5], v[2:3], 0, s[26:27]
	global_load_lds_dwordx4 v[4:5], off
	v_lshl_add_u64 v[2:3], v[2:3], 0, s[28:29]
	s_add_i32 m0, s34, 0x2000
	s_add_i32 s34, s35, s39
	global_load_lds_dwordx4 v[2:3], off
	s_mov_b32 m0, s34
	v_lshl_add_u64 v[2:3], s[58:59], 0, v[132:133]
	v_lshl_add_u64 v[4:5], v[2:3], 0, s[30:31]
	global_load_lds_dwordx4 v[4:5], off
	v_lshl_add_u64 v[2:3], v[2:3], 0, s[36:37]
	s_add_i32 m0, s34, 0x2000
	s_nop 0
	global_load_lds_dwordx4 v[2:3], off
	s_mov_b32 m0, s72
	v_lshl_add_u64 v[2:3], s[56:57], 0, v[130:131]
	v_lshl_add_u64 v[4:5], v[2:3], 0, s[26:27]
	global_load_lds_dwordx4 v[4:5], off
	v_lshl_add_u64 v[2:3], v[2:3], 0, s[28:29]
	s_mov_b32 m0, s73
	s_nop 0
	global_load_lds_dwordx4 v[2:3], off
	v_add_u32_e32 v168, s76, v1
	ds_read_b128 v[114:117], v168 offset:49152
	ds_read_b128 v[118:121], v168 offset:50176
	ds_read_b128 v[148:151], v168 offset:51200
	ds_read_b128 v[152:155], v168 offset:52224
	ds_read_b128 v[156:159], v168 offset:53248
	ds_read_b128 v[160:163], v168 offset:54272
	ds_read_b128 v[164:167], v168 offset:55296
	ds_read_b128 v[168:171], v168 offset:56320
	s_waitcnt vmcnt(8)
	s_waitcnt lgkmcnt(0)
	s_barrier
	s_setprio 1
	s_waitcnt lgkmcnt(0)
	v_mfma_scale_f32_16x16x128_f8f6f4 v[38:41], v[98:105], v[114:121], v[38:41], v138, v138 op_sel_hi:[0,0,0]
	v_mfma_scale_f32_16x16x128_f8f6f4 v[34:37], v[106:113], v[114:121], v[34:37], v138, v138 op_sel_hi:[0,0,0]
	v_mfma_scale_f32_16x16x128_f8f6f4 v[30:33], v[98:105], v[148:155], v[208:211], v138, v138 op_sel_hi:[0,0,0]
	v_mfma_scale_f32_16x16x128_f8f6f4 v[26:29], v[106:113], v[148:155], v[212:215], v138, v138 op_sel_hi:[0,0,0]
	v_mfma_scale_f32_16x16x128_f8f6f4 v[22:25], v[98:105], v[156:163], v[216:219], v138, v138 op_sel_hi:[0,0,0]
	v_mfma_scale_f32_16x16x128_f8f6f4 v[220:223], v[106:113], v[156:163], v[220:223], v138, v138 op_sel_hi:[0,0,0]
	v_mfma_scale_f32_16x16x128_f8f6f4 v[2:5], v[98:105], v[164:171], v[224:227], v138, v138 op_sel_hi:[0,0,0]
	v_mfma_scale_f32_16x16x128_f8f6f4 v[10:13], v[106:113], v[164:171], v[228:231], v138, v138 op_sel_hi:[0,0,0]
	s_setprio 0
	s_setprio 1
	v_mfma_scale_f32_16x16x128_f8f6f4 v[98:101], v[122:129], v[114:121], v[232:235], v138, v138 op_sel_hi:[0,0,0]
	v_mfma_scale_f32_16x16x128_f8f6f4 v[102:105], v[140:147], v[114:121], v[236:239], v138, v138 op_sel_hi:[0,0,0]
	v_mfma_scale_f32_16x16x128_f8f6f4 v[106:109], v[122:129], v[148:155], v[240:243], v138, v138 op_sel_hi:[0,0,0]
	v_mfma_scale_f32_16x16x128_f8f6f4 v[110:113], v[140:147], v[148:155], v[244:247], v138, v138 op_sel_hi:[0,0,0]
	v_mfma_scale_f32_16x16x128_f8f6f4 v[114:117], v[122:129], v[156:163], v[248:251], v138, v138 op_sel_hi:[0,0,0]
	v_mfma_scale_f32_16x16x128_f8f6f4 v[118:121], v[140:147], v[156:163], v[42:45], v138, v138 op_sel_hi:[0,0,0]
	v_mfma_scale_f32_16x16x128_f8f6f4 v[122:125], v[122:129], v[164:171], v[46:49], v138, v138 op_sel_hi:[0,0,0]
	v_mfma_scale_f32_16x16x128_f8f6f4 v[126:129], v[140:147], v[164:171], v[50:53], v138, v138 op_sel_hi:[0,0,0]
	s_setprio 0
	s_barrier
	s_add_i32 s86, s86, 2
	s_add_u32 s54, s54, 0x100
	s_addc_u32 s55, s55, 0
	s_cmp_gt_u32 s86, 13
	s_cbranch_scc0 .LBB0_1257
	s_and_b64 vcc, exec, s[40:41]
	s_cbranch_vccz .LBB0_1260
	s_barrier

.LBB0_1308:
	s_add_u32 s34, s4, 0xfffa0080
	s_addc_u32 s35, s5, -1
	s_cmp_eq_u32 s83, 12
	s_cselect_b32 s53, s45, s35
	s_cselect_b32 s52, s44, s34
	s_cselect_b32 s55, s47, s43
	s_cselect_b32 s54, s46, s41
	s_mov_b32 s34, 0xfffe0000
	s_mov_b32 s35, -1
	v_lshl_add_u64 v[192:193], s[4:5], 0, v[130:131]
	v_lshl_add_u64 v[192:193], v[192:193], 0, s[34:35]
	s_add_i32 m0, s51, 0xc000
	s_nop 0
	global_load_lds_dwordx4 v[192:193], off
	s_add_i32 m0, s51, 0xe000
	s_nop 0
	global_load_lds_dwordx4 v130, s[4:5]
	v_add_u32_e32 v133, s71, v1
	v_add_u32_e32 v148, s74, v133
	v_add_u32_e32 v133, s75, v133
	ds_read_b128 v[136:139], v148
	ds_read_b128 v[140:143], v148 offset:1024
	ds_read_b128 v[144:147], v148 offset:2048
	ds_read_b128 v[148:151], v148 offset:3072
	ds_read_b128 v[152:155], v133
	ds_read_b128 v[156:159], v133 offset:1024
	ds_read_b128 v[160:163], v133 offset:2048
	ds_read_b128 v[164:167], v133 offset:3072
	v_add_u32_e32 v133, s72, v1
	ds_read_b128 v[168:171], v133
	ds_read_b128 v[172:175], v133 offset:1024
	ds_read_b128 v[176:179], v133 offset:2048
	ds_read_b128 v[180:183], v133 offset:3072
	ds_read_b128 v[184:187], v133 offset:4096
	ds_read_b128 v[188:191], v133 offset:5120
	ds_read_b128 v[196:199], v133 offset:6144
	ds_read_b128 v[200:203], v133 offset:7168
	s_waitcnt vmcnt(8)
	s_waitcnt lgkmcnt(0)
	s_barrier
	s_setprio 1
	s_waitcnt lgkmcnt(0)
	v_mfma_scale_f32_16x16x128_f8f6f4 v[126:129], v[136:143], v[168:175], v[126:129], v134, v134 op_sel_hi:[0,0,0]
	v_mfma_scale_f32_16x16x128_f8f6f4 v[122:125], v[144:151], v[168:175], v[122:125], v134, v134 op_sel_hi:[0,0,0]
	v_mfma_scale_f32_16x16x128_f8f6f4 v[110:113], v[136:143], v[176:183], v[110:113], v134, v134 op_sel_hi:[0,0,0]
	v_mfma_scale_f32_16x16x128_f8f6f4 v[106:109], v[144:151], v[176:183], v[106:109], v134, v134 op_sel_hi:[0,0,0]
	v_mfma_scale_f32_16x16x128_f8f6f4 v[192:195], v[136:143], v[184:191], v[94:97], v134, v134 op_sel_hi:[0,0,0]
	v_mfma_scale_f32_16x16x128_f8f6f4 v[204:207], v[144:151], v[184:191], v[90:93], v134, v134 op_sel_hi:[0,0,0]
	v_mfma_scale_f32_16x16x128_f8f6f4 v[208:211], v[136:143], v[196:203], v[78:81], v134, v134 op_sel_hi:[0,0,0]
	v_mfma_scale_f32_16x16x128_f8f6f4 v[212:215], v[144:151], v[196:203], v[74:77], v134, v134 op_sel_hi:[0,0,0]
	s_setprio 0
	s_setprio 1
	v_mfma_scale_f32_16x16x128_f8f6f4 v[118:121], v[152:159], v[168:175], v[118:121], v134, v134 op_sel_hi:[0,0,0]
	v_mfma_scale_f32_16x16x128_f8f6f4 v[114:117], v[160:167], v[168:175], v[114:117], v134, v134 op_sel_hi:[0,0,0]
	v_mfma_scale_f32_16x16x128_f8f6f4 v[102:105], v[152:159], v[176:183], v[102:105], v134, v134 op_sel_hi:[0,0,0]
	v_mfma_scale_f32_16x16x128_f8f6f4 v[98:101], v[160:167], v[176:183], v[98:101], v134, v134 op_sel_hi:[0,0,0]
	v_mfma_scale_f32_16x16x128_f8f6f4 v[168:171], v[152:159], v[184:191], v[86:89], v134, v134 op_sel_hi:[0,0,0]
	v_mfma_scale_f32_16x16x128_f8f6f4 v[172:175], v[160:167], v[184:191], v[82:85], v134, v134 op_sel_hi:[0,0,0]
	v_mfma_scale_f32_16x16x128_f8f6f4 v[176:179], v[152:159], v[196:203], v[66:69], v134, v134 op_sel_hi:[0,0,0]
	v_mfma_scale_f32_16x16x128_f8f6f4 v[180:183], v[160:167], v[196:203], v[70:73], v134, v134 op_sel_hi:[0,0,0]
	s_setprio 0
	s_barrier
	v_mov_b32_e32 v133, v131
	s_add_i32 s34, s74, s62
	s_mov_b32 m0, s34
	v_lshl_add_u64 v[184:185], s[54:55], 0, v[132:133]
	global_load_lds_dwordx4 v132, s[54:55]
	v_lshl_add_u64 v[184:185], v[184:185], 0, s[8:9]
	s_add_i32 m0, s34, 0x2000
	s_add_i32 s34, s75, s62
	global_load_lds_dwordx4 v[184:185], off
	s_mov_b32 m0, s34
	v_lshl_add_u64 v[184:185], s[54:55], 0, v[132:133]
	v_lshl_add_u64 v[186:187], v[184:185], 0, s[12:13]
	global_load_lds_dwordx4 v[186:187], off
	v_lshl_add_u64 v[184:185], v[184:185], 0, s[14:15]
	s_add_i32 m0, s34, 0x2000
	s_nop 0
	global_load_lds_dwordx4 v[184:185], off
	s_mov_b32 m0, s51
	v_lshl_add_u64 v[184:185], s[52:53], 0, v[130:131]
	global_load_lds_dwordx4 v130, s[52:53]
	v_lshl_add_u64 v[184:185], v[184:185], 0, s[8:9]
	s_mov_b32 m0, s64
	s_nop 0
	global_load_lds_dwordx4 v[184:185], off
	v_add_u32_e32 v94, s72, v1
	ds_read_b128 v[66:69], v94 offset:16384
	ds_read_b128 v[70:73], v94 offset:17408
	ds_read_b128 v[74:77], v94 offset:18432
	ds_read_b128 v[78:81], v94 offset:19456
	ds_read_b128 v[82:85], v94 offset:20480
	ds_read_b128 v[86:89], v94 offset:21504
	ds_read_b128 v[90:93], v94 offset:22528
	ds_read_b128 v[94:97], v94 offset:23552
	s_waitcnt vmcnt(8)
	s_waitcnt lgkmcnt(0)
	s_barrier
	s_setprio 1
	s_waitcnt lgkmcnt(0)
	v_mfma_scale_f32_16x16x128_f8f6f4 v[62:65], v[136:143], v[66:73], v[62:65], v134, v134 op_sel_hi:[0,0,0]
	v_mfma_scale_f32_16x16x128_f8f6f4 v[58:61], v[144:151], v[66:73], v[58:61], v134, v134 op_sel_hi:[0,0,0]
	v_mfma_scale_f32_16x16x128_f8f6f4 v[10:13], v[136:143], v[90:97], v[10:13], v134, v134 op_sel_hi:[0,0,0]
	v_mfma_scale_f32_16x16x128_f8f6f4 v[184:187], v[136:143], v[74:81], v[46:49], v134, v134 op_sel_hi:[0,0,0]
	v_mfma_scale_f32_16x16x128_f8f6f4 v[188:191], v[144:151], v[74:81], v[42:45], v134, v134 op_sel_hi:[0,0,0]
	v_mfma_scale_f32_16x16x128_f8f6f4 v[196:199], v[136:143], v[82:89], v[30:33], v134, v134 op_sel_hi:[0,0,0]
	v_mfma_scale_f32_16x16x128_f8f6f4 v[200:203], v[144:151], v[82:89], v[26:29], v134, v134 op_sel_hi:[0,0,0]
	v_mfma_scale_f32_16x16x128_f8f6f4 v[216:219], v[144:151], v[90:97], v[14:17], v134, v134 op_sel_hi:[0,0,0]
	s_setprio 0
	s_setprio 1
	v_mfma_scale_f32_16x16x128_f8f6f4 v[54:57], v[152:159], v[66:73], v[54:57], v134, v134 op_sel_hi:[0,0,0]
	v_mfma_scale_f32_16x16x128_f8f6f4 v[220:223], v[160:167], v[66:73], v[50:53], v134, v134 op_sel_hi:[0,0,0]
	v_mfma_scale_f32_16x16x128_f8f6f4 v[224:227], v[152:159], v[74:81], v[38:41], v134, v134 op_sel_hi:[0,0,0]
	v_mfma_scale_f32_16x16x128_f8f6f4 v[228:231], v[160:167], v[74:81], v[34:37], v134, v134 op_sel_hi:[0,0,0]
	v_mfma_scale_f32_16x16x128_f8f6f4 v[232:235], v[152:159], v[82:89], v[22:25], v134, v134 op_sel_hi:[0,0,0]
	v_mfma_scale_f32_16x16x128_f8f6f4 v[236:239], v[160:167], v[82:89], v[18:21], v134, v134 op_sel_hi:[0,0,0]
	v_mfma_scale_f32_16x16x128_f8f6f4 v[240:243], v[152:159], v[90:97], v[6:9], v134, v134 op_sel_hi:[0,0,0]
	v_mfma_scale_f32_16x16x128_f8f6f4 v[244:247], v[160:167], v[90:97], v[2:5], v134, v134 op_sel_hi:[0,0,0]
	s_setprio 0
	s_barrier
	s_mov_b32 m0, s65
	v_lshl_add_u64 v[66:67], s[52:53], 0, v[130:131]
	v_lshl_add_u64 v[68:69], v[66:67], 0, s[12:13]
	global_load_lds_dwordx4 v[68:69], off
	v_lshl_add_u64 v[66:67], v[66:67], 0, s[14:15]
	s_mov_b32 m0, s66
	s_nop 0
	global_load_lds_dwordx4 v[66:67], off
	s_add_i32 s34, 0, 0x18000
	v_add_u32_e32 v22, s71, v1
	s_add_i32 s35, 0, 0x1c000
	v_add_u32_e32 v18, s34, v22
	v_add_u32_e32 v22, s35, v22
	ds_read_b128 v[2:5], v18
	ds_read_b128 v[6:9], v18 offset:1024
	ds_read_b128 v[14:17], v18 offset:2048
	ds_read_b128 v[18:21], v18 offset:3072
	ds_read_b128 v[136:139], v22
	ds_read_b128 v[140:143], v22 offset:1024
	ds_read_b128 v[144:147], v22 offset:2048
	ds_read_b128 v[148:151], v22 offset:3072
	v_add_u32_e32 v50, s72, v1
	ds_read_b128 v[22:25], v50 offset:32768
	ds_read_b128 v[26:29], v50 offset:33792
	ds_read_b128 v[30:33], v50 offset:34816
	ds_read_b128 v[34:37], v50 offset:35840
	ds_read_b128 v[38:41], v50 offset:36864
	ds_read_b128 v[42:45], v50 offset:37888
	ds_read_b128 v[46:49], v50 offset:38912
	ds_read_b128 v[50:53], v50 offset:39936
	s_waitcnt vmcnt(8)
	s_waitcnt lgkmcnt(0)
	s_barrier
	s_setprio 1
	s_waitcnt lgkmcnt(0)
	v_mfma_scale_f32_16x16x128_f8f6f4 v[126:129], v[2:9], v[22:29], v[126:129], v134, v134 op_sel_hi:[0,0,0]
	v_mfma_scale_f32_16x16x128_f8f6f4 v[122:125], v[14:21], v[22:29], v[122:125], v134, v134 op_sel_hi:[0,0,0]
	v_mfma_scale_f32_16x16x128_f8f6f4 v[110:113], v[2:9], v[30:37], v[110:113], v134, v134 op_sel_hi:[0,0,0]
	v_mfma_scale_f32_16x16x128_f8f6f4 v[106:109], v[14:21], v[30:37], v[106:109], v134, v134 op_sel_hi:[0,0,0]
	v_mfma_scale_f32_16x16x128_f8f6f4 v[94:97], v[2:9], v[38:45], v[192:195], v134, v134 op_sel_hi:[0,0,0]
	v_mfma_scale_f32_16x16x128_f8f6f4 v[90:93], v[14:21], v[38:45], v[204:207], v134, v134 op_sel_hi:[0,0,0]
	v_mfma_scale_f32_16x16x128_f8f6f4 v[78:81], v[2:9], v[46:53], v[208:211], v134, v134 op_sel_hi:[0,0,0]
	v_mfma_scale_f32_16x16x128_f8f6f4 v[74:77], v[14:21], v[46:53], v[212:215], v134, v134 op_sel_hi:[0,0,0]
	s_setprio 0
	s_setprio 1
	v_mfma_scale_f32_16x16x128_f8f6f4 v[118:121], v[136:143], v[22:29], v[118:121], v134, v134 op_sel_hi:[0,0,0]
	v_mfma_scale_f32_16x16x128_f8f6f4 v[114:117], v[144:151], v[22:29], v[114:117], v134, v134 op_sel_hi:[0,0,0]
	v_mfma_scale_f32_16x16x128_f8f6f4 v[102:105], v[136:143], v[30:37], v[102:105], v134, v134 op_sel_hi:[0,0,0]
	v_mfma_scale_f32_16x16x128_f8f6f4 v[98:101], v[144:151], v[30:37], v[98:101], v134, v134 op_sel_hi:[0,0,0]
	v_mfma_scale_f32_16x16x128_f8f6f4 v[86:89], v[136:143], v[38:45], v[168:171], v134, v134 op_sel_hi:[0,0,0]
	v_mfma_scale_f32_16x16x128_f8f6f4 v[82:85], v[144:151], v[38:45], v[172:175], v134, v134 op_sel_hi:[0,0,0]
	v_mfma_scale_f32_16x16x128_f8f6f4 v[66:69], v[136:143], v[46:53], v[176:179], v134, v134 op_sel_hi:[0,0,0]
	v_mfma_scale_f32_16x16x128_f8f6f4 v[70:73], v[144:151], v[46:53], v[180:183], v134, v134 op_sel_hi:[0,0,0]
	s_setprio 0
	s_barrier
	s_add_i32 s34, s34, s62
	s_mov_b32 m0, s34
	v_lshl_add_u64 v[22:23], s[54:55], 0, v[132:133]
	v_lshl_add_u64 v[24:25], v[22:23], 0, s[20:21]
	global_load_lds_dwordx4 v[24:25], off
	v_lshl_add_u64 v[22:23], v[22:23], 0, s[22:23]
	s_add_i32 m0, s34, 0x2000
	s_add_i32 s34, s35, s62
	global_load_lds_dwordx4 v[22:23], off
	s_mov_b32 m0, s34
	v_lshl_add_u64 v[22:23], s[54:55], 0, v[132:133]
	v_lshl_add_u64 v[24:25], v[22:23], 0, s[24:25]
	global_load_lds_dwordx4 v[24:25], off
	v_lshl_add_u64 v[22:23], v[22:23], 0, s[26:27]
	s_add_i32 m0, s34, 0x2000
	s_nop 0
	global_load_lds_dwordx4 v[22:23], off
	s_mov_b32 m0, s69
	v_lshl_add_u64 v[22:23], s[52:53], 0, v[130:131]
	v_lshl_add_u64 v[24:25], v[22:23], 0, s[20:21]
	global_load_lds_dwordx4 v[24:25], off
	v_lshl_add_u64 v[22:23], v[22:23], 0, s[22:23]
	s_mov_b32 m0, s70
	s_nop 0
	global_load_lds_dwordx4 v[22:23], off
	v_add_u32_e32 v172, s72, v1
	ds_read_b128 v[34:37], v172 offset:49152
	ds_read_b128 v[38:41], v172 offset:50176
	ds_read_b128 v[152:155], v172 offset:51200
	ds_read_b128 v[156:159], v172 offset:52224
	ds_read_b128 v[160:163], v172 offset:53248
	ds_read_b128 v[164:167], v172 offset:54272
	ds_read_b128 v[168:171], v172 offset:55296
	ds_read_b128 v[172:175], v172 offset:56320
	s_waitcnt vmcnt(8)
	s_waitcnt lgkmcnt(0)
	s_barrier
	s_setprio 1
	s_waitcnt lgkmcnt(0)
	v_mfma_scale_f32_16x16x128_f8f6f4 v[62:65], v[2:9], v[34:41], v[62:65], v134, v134 op_sel_hi:[0,0,0]
	v_mfma_scale_f32_16x16x128_f8f6f4 v[58:61], v[14:21], v[34:41], v[58:61], v134, v134 op_sel_hi:[0,0,0]
	v_mfma_scale_f32_16x16x128_f8f6f4 v[46:49], v[2:9], v[152:159], v[184:187], v134, v134 op_sel_hi:[0,0,0]
	v_mfma_scale_f32_16x16x128_f8f6f4 v[42:45], v[14:21], v[152:159], v[188:191], v134, v134 op_sel_hi:[0,0,0]
	v_mfma_scale_f32_16x16x128_f8f6f4 v[30:33], v[2:9], v[160:167], v[196:199], v134, v134 op_sel_hi:[0,0,0]
	v_mfma_scale_f32_16x16x128_f8f6f4 v[26:29], v[14:21], v[160:167], v[200:203], v134, v134 op_sel_hi:[0,0,0]
	v_mfma_scale_f32_16x16x128_f8f6f4 v[10:13], v[2:9], v[168:175], v[10:13], v134, v134 op_sel_hi:[0,0,0]
	v_mfma_scale_f32_16x16x128_f8f6f4 v[14:17], v[14:21], v[168:175], v[216:219], v134, v134 op_sel_hi:[0,0,0]
	s_setprio 0
	s_setprio 1
	v_mfma_scale_f32_16x16x128_f8f6f4 v[54:57], v[136:143], v[34:41], v[54:57], v134, v134 op_sel_hi:[0,0,0]
	v_mfma_scale_f32_16x16x128_f8f6f4 v[50:53], v[144:151], v[34:41], v[220:223], v134, v134 op_sel_hi:[0,0,0]
	v_mfma_scale_f32_16x16x128_f8f6f4 v[38:41], v[136:143], v[152:159], v[224:227], v134, v134 op_sel_hi:[0,0,0]
	v_mfma_scale_f32_16x16x128_f8f6f4 v[34:37], v[144:151], v[152:159], v[228:231], v134, v134 op_sel_hi:[0,0,0]
	v_mfma_scale_f32_16x16x128_f8f6f4 v[22:25], v[136:143], v[160:167], v[232:235], v134, v134 op_sel_hi:[0,0,0]
	v_mfma_scale_f32_16x16x128_f8f6f4 v[18:21], v[144:151], v[160:167], v[236:239], v134, v134 op_sel_hi:[0,0,0]
	v_mfma_scale_f32_16x16x128_f8f6f4 v[6:9], v[136:143], v[168:175], v[240:243], v134, v134 op_sel_hi:[0,0,0]
	v_mfma_scale_f32_16x16x128_f8f6f4 v[2:5], v[144:151], v[168:175], v[244:247], v134, v134 op_sel_hi:[0,0,0]
	s_setprio 0
	s_barrier
	s_add_i32 s83, s83, 2
	s_add_u32 s4, s4, 0x100
	s_addc_u32 s5, s5, 0
	s_add_u32 s41, s41, 0x100
	s_addc_u32 s43, s43, 0
	s_cmp_gt_u32 s83, 13
	s_cbranch_scc0 .LBB0_1308
	s_and_b64 vcc, exec, s[28:29]
	s_cbranch_vccz .LBB0_1311
	s_barrier
